# GEMM K-loops: priority drop/raise pair after every 8 MFMAs instead of every 16 (the mid-cluster flip proved load-bearing)
# speedup vs baseline: 1.0027x; 1.0027x over previous
.LBB0_121:
	s_add_u32 s38, s12, 0x80
	s_addc_u32 s39, s13, 0
	s_waitcnt vmcnt(8)
	s_and_b64 s[14:15], s[14:15], exec
	s_waitcnt lgkmcnt(0)
	s_cselect_b32 s14, s57, s58
	s_cselect_b32 s41, s31, s39
	s_cselect_b32 s40, s30, s38
	s_cselect_b32 s15, s7, s59
	s_add_u32 s38, s14, 0x8000
	s_addc_u32 s39, s15, 0
	s_barrier
	s_setprio 1
	s_waitcnt lgkmcnt(0)
	v_mfma_f32_16x16x32_bf16 v[64:67], v[104:107], v[128:131], v[64:67]
	v_mfma_f32_16x16x32_bf16 v[60:63], v[112:115], v[128:131], v[60:63]
	v_mfma_f32_16x16x32_bf16 v[56:59], v[104:107], v[120:123], v[56:59]
	v_mfma_f32_16x16x32_bf16 v[52:55], v[112:115], v[120:123], v[52:55]
	v_mfma_f32_16x16x32_bf16 v[40:43], v[104:107], v[96:99], v[40:43]
	v_mfma_f32_16x16x32_bf16 v[36:39], v[112:115], v[96:99], v[36:39]
	v_mfma_f32_16x16x32_bf16 v[24:27], v[104:107], v[88:91], v[24:27]
	v_mfma_f32_16x16x32_bf16 v[20:23], v[112:115], v[88:91], v[20:23]
	s_setprio 0
	s_setprio 1
	v_mfma_f32_16x16x32_bf16 v[64:67], v[108:111], v[132:135], v[64:67]
	v_mfma_f32_16x16x32_bf16 v[60:63], v[116:119], v[132:135], v[60:63]
	v_mfma_f32_16x16x32_bf16 v[56:59], v[108:111], v[124:127], v[56:59]
	v_mfma_f32_16x16x32_bf16 v[52:55], v[116:119], v[124:127], v[52:55]
	v_mfma_f32_16x16x32_bf16 v[40:43], v[108:111], v[100:103], v[40:43]
	v_mfma_f32_16x16x32_bf16 v[36:39], v[116:119], v[100:103], v[36:39]
	v_mfma_f32_16x16x32_bf16 v[24:27], v[108:111], v[92:95], v[24:27]
	v_mfma_f32_16x16x32_bf16 v[20:23], v[116:119], v[92:95], v[20:23]
	s_setprio 0
	s_setprio 1
	v_mfma_f32_16x16x32_bf16 v[48:51], v[68:71], v[128:131], v[48:51]
	v_mfma_f32_16x16x32_bf16 v[44:47], v[76:79], v[128:131], v[44:47]
	v_mfma_f32_16x16x32_bf16 v[32:35], v[68:71], v[120:123], v[32:35]
	v_mfma_f32_16x16x32_bf16 v[28:31], v[76:79], v[120:123], v[28:31]
	v_mfma_f32_16x16x32_bf16 v[16:19], v[68:71], v[96:99], v[16:19]
	v_mfma_f32_16x16x32_bf16 v[12:15], v[76:79], v[96:99], v[12:15]
	v_mfma_f32_16x16x32_bf16 v[8:11], v[68:71], v[88:91], v[8:11]
	v_mfma_f32_16x16x32_bf16 v[4:7], v[76:79], v[88:91], v[4:7]
	s_setprio 0
	s_setprio 1
	v_mfma_f32_16x16x32_bf16 v[48:51], v[72:75], v[132:135], v[48:51]
	v_mfma_f32_16x16x32_bf16 v[44:47], v[80:83], v[132:135], v[44:47]
	v_mfma_f32_16x16x32_bf16 v[32:35], v[72:75], v[124:127], v[32:35]
	v_mfma_f32_16x16x32_bf16 v[28:31], v[80:83], v[124:127], v[28:31]
	v_mfma_f32_16x16x32_bf16 v[16:19], v[72:75], v[100:103], v[16:19]
	v_mfma_f32_16x16x32_bf16 v[12:15], v[80:83], v[100:103], v[12:15]
	v_mfma_f32_16x16x32_bf16 v[8:11], v[72:75], v[92:95], v[8:11]
	v_mfma_f32_16x16x32_bf16 v[4:7], v[80:83], v[92:95], v[4:7]
	s_setprio 0
	s_barrier
	s_mov_b32 m0, s43
	v_lshl_add_u64 v[68:69], s[14:15], 0, v[138:139]
	s_add_u32 s62, s14, 0x4000
	global_load_lds_dwordx4 v[68:69], off
	v_lshl_add_u64 v[68:69], s[14:15], 0, v[136:137]
	s_mov_b32 m0, s44
	s_addc_u32 s63, s15, 0
	global_load_lds_dwordx4 v[68:69], off
	v_lshl_add_u64 v[68:69], s[62:63], 0, v[138:139]
	s_mov_b32 m0, s45
	v_mov_b32_e32 v143, v3
	global_load_lds_dwordx4 v[68:69], off
	v_lshl_add_u64 v[68:69], s[62:63], 0, v[136:137]
	s_mov_b32 m0, s47
	v_lshl_add_u64 v[166:167], s[40:41], 0, v[2:3]
	global_load_lds_dwordx4 v[68:69], off
	s_mov_b32 m0, s42
	v_lshl_add_u64 v[168:169], s[40:41], 0, v[142:143]
	global_load_lds_dwordx4 v2, s[40:41]
	s_mov_b32 m0, s48
	s_nop 0
	global_load_lds_dwordx4 v142, s[40:41]
	s_waitcnt vmcnt(8)
	s_waitcnt lgkmcnt(0)
	s_barrier
	s_barrier
	s_add_i32 s61, 0, 0x18000
	s_add_i32 s62, 0, 0x1c000
	v_add_u32_e32 v80, s61, v160
	v_add_u32_e32 v100, s62, v160
	ds_read_b128 v[68:71], v80
	ds_read_b128 v[72:75], v80 offset:1024
	ds_read_b128 v[76:79], v80 offset:2048
	ds_read_b128 v[80:83], v80 offset:3072
	ds_read_b128 v[88:91], v100
	ds_read_b128 v[92:95], v100 offset:1024
	ds_read_b128 v[96:99], v100 offset:2048
	ds_read_b128 v[100:103], v100 offset:3072
	s_mov_b32 m0, s49
	v_lshl_add_u64 v[154:155], s[40:41], 0, v[154:155]
	ds_read_b128 v[104:107], v163 offset:32768
	ds_read_b128 v[108:111], v163 offset:33792
	ds_read_b128 v[112:115], v163 offset:34816
	ds_read_b128 v[116:119], v163 offset:35840
	ds_read_b128 v[120:123], v163 offset:36864
	ds_read_b128 v[124:127], v163 offset:37888
	ds_read_b128 v[128:131], v163 offset:38912
	ds_read_b128 v[132:135], v163 offset:39936
	global_load_lds_dwordx4 v[154:155], off
	v_lshl_add_u64 v[152:153], s[40:41], 0, v[152:153]
	s_mov_b32 m0, s50
	s_nop 0
	global_load_lds_dwordx4 v[152:153], off
	s_waitcnt vmcnt(8)
	s_waitcnt lgkmcnt(0)
	s_barrier
	s_setprio 1
	s_waitcnt lgkmcnt(0)
	v_mfma_f32_16x16x32_bf16 v[64:67], v[68:71], v[104:107], v[64:67]
	v_mfma_f32_16x16x32_bf16 v[60:63], v[76:79], v[104:107], v[60:63]
	v_mfma_f32_16x16x32_bf16 v[56:59], v[68:71], v[112:115], v[56:59]
	v_mfma_f32_16x16x32_bf16 v[52:55], v[76:79], v[112:115], v[52:55]
	v_mfma_f32_16x16x32_bf16 v[40:43], v[68:71], v[120:123], v[40:43]
	v_mfma_f32_16x16x32_bf16 v[36:39], v[76:79], v[120:123], v[36:39]
	v_mfma_f32_16x16x32_bf16 v[24:27], v[68:71], v[128:131], v[24:27]
	v_mfma_f32_16x16x32_bf16 v[20:23], v[76:79], v[128:131], v[20:23]
	s_setprio 0
	s_setprio 1
	v_mfma_f32_16x16x32_bf16 v[64:67], v[72:75], v[108:111], v[64:67]
	v_mfma_f32_16x16x32_bf16 v[60:63], v[80:83], v[108:111], v[60:63]
	v_mfma_f32_16x16x32_bf16 v[56:59], v[72:75], v[116:119], v[56:59]
	v_mfma_f32_16x16x32_bf16 v[52:55], v[80:83], v[116:119], v[52:55]
	v_mfma_f32_16x16x32_bf16 v[40:43], v[72:75], v[124:127], v[40:43]
	v_mfma_f32_16x16x32_bf16 v[36:39], v[80:83], v[124:127], v[36:39]
	v_mfma_f32_16x16x32_bf16 v[24:27], v[72:75], v[132:135], v[24:27]
	v_mfma_f32_16x16x32_bf16 v[20:23], v[80:83], v[132:135], v[20:23]
	s_setprio 0
	s_setprio 1
	v_mfma_f32_16x16x32_bf16 v[48:51], v[88:91], v[104:107], v[48:51]
	v_mfma_f32_16x16x32_bf16 v[44:47], v[96:99], v[104:107], v[44:47]
	v_mfma_f32_16x16x32_bf16 v[32:35], v[88:91], v[112:115], v[32:35]
	v_mfma_f32_16x16x32_bf16 v[28:31], v[96:99], v[112:115], v[28:31]
	v_mfma_f32_16x16x32_bf16 v[16:19], v[88:91], v[120:123], v[16:19]
	v_mfma_f32_16x16x32_bf16 v[12:15], v[96:99], v[120:123], v[12:15]
	v_mfma_f32_16x16x32_bf16 v[8:11], v[88:91], v[128:131], v[8:11]
	v_mfma_f32_16x16x32_bf16 v[4:7], v[96:99], v[128:131], v[4:7]
	s_setprio 0
	s_setprio 1
	v_mfma_f32_16x16x32_bf16 v[48:51], v[92:95], v[108:111], v[48:51]
	v_mfma_f32_16x16x32_bf16 v[44:47], v[100:103], v[108:111], v[44:47]
	v_mfma_f32_16x16x32_bf16 v[32:35], v[92:95], v[116:119], v[32:35]
	v_mfma_f32_16x16x32_bf16 v[28:31], v[100:103], v[116:119], v[28:31]
	v_mfma_f32_16x16x32_bf16 v[16:19], v[92:95], v[124:127], v[16:19]
	v_mfma_f32_16x16x32_bf16 v[12:15], v[100:103], v[124:127], v[12:15]
	v_mfma_f32_16x16x32_bf16 v[8:11], v[92:95], v[132:135], v[8:11]
	v_mfma_f32_16x16x32_bf16 v[4:7], v[100:103], v[132:135], v[4:7]
	s_setprio 0
	s_barrier
	s_add_i32 s40, s61, s33
	v_lshl_add_u64 v[68:69], s[38:39], 0, v[138:139]
	s_mov_b32 m0, s40
	s_nop 0
	global_load_lds_dwordx4 v[68:69], off
	s_add_i32 m0, s40, 0x2000
	s_add_u32 s14, s14, 0xc000
	v_lshl_add_u64 v[68:69], s[38:39], 0, v[136:137]
	s_addc_u32 s15, s15, 0
	s_add_i32 s38, s62, s33
	global_load_lds_dwordx4 v[68:69], off
	v_lshl_add_u64 v[68:69], s[14:15], 0, v[138:139]
	s_mov_b32 m0, s38
	s_nop 0
	global_load_lds_dwordx4 v[68:69], off
	v_lshl_add_u64 v[68:69], s[14:15], 0, v[136:137]
	s_add_i32 m0, s38, 0x2000
	s_nop 0
	global_load_lds_dwordx4 v[68:69], off
	v_lshl_add_u64 v[68:69], v[166:167], 0, s[36:37]
	s_mov_b32 m0, s51
	s_nop 0
	global_load_lds_dwordx4 v[68:69], off
	v_lshl_add_u64 v[68:69], v[168:169], 0, s[36:37]
	s_mov_b32 m0, s52
	s_nop 0
	global_load_lds_dwordx4 v[68:69], off
	s_waitcnt vmcnt(8)
	s_waitcnt lgkmcnt(0)
	s_barrier
	s_barrier
	s_add_i32 s60, s60, 2
	s_add_u32 s58, s58, 0x10000
	s_addc_u32 s59, s59, 0
	s_add_u32 s12, s12, 0x100
	s_addc_u32 s13, s13, 0
	s_cmp_gt_u32 s60, 29
	s_cbranch_scc1 .LBB0_124

.LBB0_144:
	s_add_u32 s40, s14, 0x80
	s_addc_u32 s41, s15, 0
	s_waitcnt vmcnt(8)
	s_and_b64 s[38:39], s[38:39], exec
	s_waitcnt lgkmcnt(0)
	s_cselect_b32 s38, s13, s60
	s_cselect_b32 s43, s31, s41
	s_cselect_b32 s42, s30, s40
	s_cselect_b32 s39, s9, s61
	s_add_u32 s40, s38, 0x8000
	s_addc_u32 s41, s39, 0
	s_barrier
	s_setprio 1
	s_waitcnt lgkmcnt(0)
	v_mfma_f32_16x16x32_bf16 v[132:135], v[152:155], v[192:195], v[132:135]
	v_mfma_f32_16x16x32_bf16 v[128:131], v[160:163], v[192:195], v[128:131]
	v_mfma_f32_16x16x32_bf16 v[124:127], v[152:155], v[184:187], v[124:127]
	v_mfma_f32_16x16x32_bf16 v[116:119], v[160:163], v[184:187], v[116:119]
	v_mfma_f32_16x16x32_bf16 v[108:111], v[152:155], v[176:179], v[108:111]
	v_mfma_f32_16x16x32_bf16 v[100:103], v[160:163], v[176:179], v[100:103]
	v_mfma_f32_16x16x32_bf16 v[92:95], v[152:155], v[168:171], v[92:95]
	v_mfma_f32_16x16x32_bf16 v[80:83], v[160:163], v[168:171], v[80:83]
	s_setprio 0
	s_setprio 1
	v_mfma_f32_16x16x32_bf16 v[132:135], v[156:159], v[196:199], v[132:135]
	v_mfma_f32_16x16x32_bf16 v[128:131], v[164:167], v[196:199], v[128:131]
	v_mfma_f32_16x16x32_bf16 v[124:127], v[156:159], v[188:191], v[124:127]
	v_mfma_f32_16x16x32_bf16 v[116:119], v[164:167], v[188:191], v[116:119]
	v_mfma_f32_16x16x32_bf16 v[108:111], v[156:159], v[180:183], v[108:111]
	v_mfma_f32_16x16x32_bf16 v[100:103], v[164:167], v[180:183], v[100:103]
	v_mfma_f32_16x16x32_bf16 v[92:95], v[156:159], v[172:175], v[92:95]
	v_mfma_f32_16x16x32_bf16 v[80:83], v[164:167], v[172:175], v[80:83]
	s_setprio 0
	s_setprio 1
	v_mfma_f32_16x16x32_bf16 v[120:123], v[136:139], v[192:195], v[120:123]
	v_mfma_f32_16x16x32_bf16 v[112:115], v[144:147], v[192:195], v[112:115]
	v_mfma_f32_16x16x32_bf16 v[104:107], v[136:139], v[184:187], v[104:107]
	v_mfma_f32_16x16x32_bf16 v[96:99], v[144:147], v[184:187], v[96:99]
	v_mfma_f32_16x16x32_bf16 v[88:91], v[136:139], v[176:179], v[88:91]
	v_mfma_f32_16x16x32_bf16 v[76:79], v[144:147], v[176:179], v[76:79]
	v_mfma_f32_16x16x32_bf16 v[72:75], v[136:139], v[168:171], v[72:75]
	v_mfma_f32_16x16x32_bf16 v[68:71], v[144:147], v[168:171], v[68:71]
	s_setprio 0
	s_setprio 1
	v_mfma_f32_16x16x32_bf16 v[120:123], v[140:143], v[196:199], v[120:123]
	v_mfma_f32_16x16x32_bf16 v[112:115], v[148:151], v[196:199], v[112:115]
	v_mfma_f32_16x16x32_bf16 v[104:107], v[140:143], v[188:191], v[104:107]
	v_mfma_f32_16x16x32_bf16 v[96:99], v[148:151], v[188:191], v[96:99]
	v_mfma_f32_16x16x32_bf16 v[88:91], v[140:143], v[180:183], v[88:91]
	v_mfma_f32_16x16x32_bf16 v[76:79], v[148:151], v[180:183], v[76:79]
	v_mfma_f32_16x16x32_bf16 v[72:75], v[140:143], v[172:175], v[72:75]
	v_mfma_f32_16x16x32_bf16 v[68:71], v[148:151], v[172:175], v[68:71]
	s_setprio 0
	s_barrier
	s_mov_b32 m0, s48
	v_lshl_add_u64 v[204:205], s[38:39], 0, v[210:211]
	s_add_u32 s64, s38, 0x4000
	ds_read_b128 v[168:171], v244 offset:16384
	ds_read_b128 v[172:175], v244 offset:17408
	ds_read_b128 v[176:179], v244 offset:18432
	ds_read_b128 v[180:183], v244 offset:19456
	ds_read_b128 v[184:187], v244 offset:20480
	ds_read_b128 v[188:191], v244 offset:21504
	ds_read_b128 v[192:195], v244 offset:22528
	ds_read_b128 v[196:199], v244 offset:23552
	global_load_lds_dwordx4 v[204:205], off
	v_lshl_add_u64 v[204:205], s[38:39], 0, v[208:209]
	s_mov_b32 m0, s49
	s_addc_u32 s65, s39, 0
	global_load_lds_dwordx4 v[204:205], off
	v_lshl_add_u64 v[204:205], s[64:65], 0, v[210:211]
	s_mov_b32 m0, s50
	v_mov_b32_e32 v215, v3
	global_load_lds_dwordx4 v[204:205], off
	v_lshl_add_u64 v[204:205], s[64:65], 0, v[208:209]
	s_mov_b32 m0, s51
	v_lshl_add_u64 v[248:249], s[42:43], 0, v[214:215]
	global_load_lds_dwordx4 v[204:205], off
	s_mov_b32 m0, s47
	v_lshl_add_u64 v[204:205], s[42:43], 0, v[2:3]
	global_load_lds_dwordx4 v2, s[42:43]
	s_mov_b32 m0, s52
	s_nop 0
	global_load_lds_dwordx4 v214, s[42:43]
	s_waitcnt vmcnt(8)
	s_waitcnt lgkmcnt(0)
	s_barrier
	s_setprio 1
	s_waitcnt lgkmcnt(0)
	v_mfma_f32_16x16x32_bf16 v[64:67], v[152:155], v[168:171], v[64:67]
	v_mfma_f32_16x16x32_bf16 v[60:63], v[160:163], v[168:171], v[60:63]
	v_mfma_f32_16x16x32_bf16 v[56:59], v[152:155], v[176:179], v[56:59]
	v_mfma_f32_16x16x32_bf16 v[48:51], v[160:163], v[176:179], v[48:51]
	v_mfma_f32_16x16x32_bf16 v[40:43], v[152:155], v[184:187], v[40:43]
	v_mfma_f32_16x16x32_bf16 v[32:35], v[160:163], v[184:187], v[32:35]
	v_mfma_f32_16x16x32_bf16 v[24:27], v[152:155], v[192:195], v[24:27]
	v_mfma_f32_16x16x32_bf16 v[16:19], v[160:163], v[192:195], v[16:19]
	s_setprio 0
	s_setprio 1
	v_mfma_f32_16x16x32_bf16 v[64:67], v[156:159], v[172:175], v[64:67]
	v_mfma_f32_16x16x32_bf16 v[60:63], v[164:167], v[172:175], v[60:63]
	v_mfma_f32_16x16x32_bf16 v[56:59], v[156:159], v[180:183], v[56:59]
	v_mfma_f32_16x16x32_bf16 v[48:51], v[164:167], v[180:183], v[48:51]
	v_mfma_f32_16x16x32_bf16 v[40:43], v[156:159], v[188:191], v[40:43]
	v_mfma_f32_16x16x32_bf16 v[32:35], v[164:167], v[188:191], v[32:35]
	v_mfma_f32_16x16x32_bf16 v[24:27], v[156:159], v[196:199], v[24:27]
	v_mfma_f32_16x16x32_bf16 v[16:19], v[164:167], v[196:199], v[16:19]
	s_setprio 0
	s_setprio 1
	v_mfma_f32_16x16x32_bf16 v[52:55], v[136:139], v[168:171], v[52:55]
	v_mfma_f32_16x16x32_bf16 v[44:47], v[144:147], v[168:171], v[44:47]
	v_mfma_f32_16x16x32_bf16 v[36:39], v[136:139], v[176:179], v[36:39]
	v_mfma_f32_16x16x32_bf16 v[28:31], v[144:147], v[176:179], v[28:31]
	v_mfma_f32_16x16x32_bf16 v[20:23], v[136:139], v[184:187], v[20:23]
	v_mfma_f32_16x16x32_bf16 v[12:15], v[144:147], v[184:187], v[12:15]
	v_mfma_f32_16x16x32_bf16 v[8:11], v[136:139], v[192:195], v[8:11]
	v_mfma_f32_16x16x32_bf16 v[4:7], v[144:147], v[192:195], v[4:7]
	s_setprio 0
	s_setprio 1
	v_mfma_f32_16x16x32_bf16 v[52:55], v[140:143], v[172:175], v[52:55]
	v_mfma_f32_16x16x32_bf16 v[44:47], v[148:151], v[172:175], v[44:47]
	v_mfma_f32_16x16x32_bf16 v[36:39], v[140:143], v[180:183], v[36:39]
	v_mfma_f32_16x16x32_bf16 v[28:31], v[148:151], v[180:183], v[28:31]
	v_mfma_f32_16x16x32_bf16 v[20:23], v[140:143], v[188:191], v[20:23]
	v_mfma_f32_16x16x32_bf16 v[12:15], v[148:151], v[188:191], v[12:15]
	v_mfma_f32_16x16x32_bf16 v[8:11], v[140:143], v[196:199], v[8:11]
	v_mfma_f32_16x16x32_bf16 v[4:7], v[148:151], v[196:199], v[4:7]
	s_setprio 0
	s_barrier
	s_add_i32 s63, 0, 0x18000
	s_add_i32 s64, 0, 0x1c000
	v_add_u32_e32 v148, s63, v243
	v_add_u32_e32 v164, s64, v243
	ds_read_b128 v[136:139], v148
	ds_read_b128 v[140:143], v148 offset:1024
	ds_read_b128 v[144:147], v148 offset:2048
	ds_read_b128 v[148:151], v148 offset:3072
	ds_read_b128 v[152:155], v164
	ds_read_b128 v[156:159], v164 offset:1024
	ds_read_b128 v[160:163], v164 offset:2048
	ds_read_b128 v[164:167], v164 offset:3072
	s_mov_b32 m0, s53
	v_lshl_add_u64 v[226:227], s[42:43], 0, v[226:227]
	ds_read_b128 v[168:171], v244 offset:32768
	ds_read_b128 v[172:175], v244 offset:33792
	ds_read_b128 v[176:179], v244 offset:34816
	ds_read_b128 v[180:183], v244 offset:35840
	ds_read_b128 v[184:187], v244 offset:36864
	ds_read_b128 v[188:191], v244 offset:37888
	ds_read_b128 v[192:195], v244 offset:38912
	ds_read_b128 v[196:199], v244 offset:39936
	global_load_lds_dwordx4 v[226:227], off
	v_lshl_add_u64 v[224:225], s[42:43], 0, v[224:225]
	s_mov_b32 m0, s54
	s_nop 0
	global_load_lds_dwordx4 v[224:225], off
	s_waitcnt vmcnt(8)
	s_waitcnt lgkmcnt(0)
	s_barrier
	s_setprio 1
	s_waitcnt lgkmcnt(0)
	v_mfma_f32_16x16x32_bf16 v[132:135], v[136:139], v[168:171], v[132:135]
	v_mfma_f32_16x16x32_bf16 v[128:131], v[144:147], v[168:171], v[128:131]
	v_mfma_f32_16x16x32_bf16 v[124:127], v[136:139], v[176:179], v[124:127]
	v_mfma_f32_16x16x32_bf16 v[116:119], v[144:147], v[176:179], v[116:119]
	v_mfma_f32_16x16x32_bf16 v[108:111], v[136:139], v[184:187], v[108:111]
	v_mfma_f32_16x16x32_bf16 v[100:103], v[144:147], v[184:187], v[100:103]
	v_mfma_f32_16x16x32_bf16 v[92:95], v[136:139], v[192:195], v[92:95]
	v_mfma_f32_16x16x32_bf16 v[80:83], v[144:147], v[192:195], v[80:83]
	s_setprio 0
	s_setprio 1
	v_mfma_f32_16x16x32_bf16 v[132:135], v[140:143], v[172:175], v[132:135]
	v_mfma_f32_16x16x32_bf16 v[128:131], v[148:151], v[172:175], v[128:131]
	v_mfma_f32_16x16x32_bf16 v[124:127], v[140:143], v[180:183], v[124:127]
	v_mfma_f32_16x16x32_bf16 v[116:119], v[148:151], v[180:183], v[116:119]
	v_mfma_f32_16x16x32_bf16 v[108:111], v[140:143], v[188:191], v[108:111]
	v_mfma_f32_16x16x32_bf16 v[100:103], v[148:151], v[188:191], v[100:103]
	v_mfma_f32_16x16x32_bf16 v[92:95], v[140:143], v[196:199], v[92:95]
	v_mfma_f32_16x16x32_bf16 v[80:83], v[148:151], v[196:199], v[80:83]
	s_setprio 0
	s_setprio 1
	v_mfma_f32_16x16x32_bf16 v[120:123], v[152:155], v[168:171], v[120:123]
	v_mfma_f32_16x16x32_bf16 v[112:115], v[160:163], v[168:171], v[112:115]
	v_mfma_f32_16x16x32_bf16 v[104:107], v[152:155], v[176:179], v[104:107]
	v_mfma_f32_16x16x32_bf16 v[96:99], v[160:163], v[176:179], v[96:99]
	v_mfma_f32_16x16x32_bf16 v[88:91], v[152:155], v[184:187], v[88:91]
	v_mfma_f32_16x16x32_bf16 v[76:79], v[160:163], v[184:187], v[76:79]
	v_mfma_f32_16x16x32_bf16 v[72:75], v[152:155], v[192:195], v[72:75]
	v_mfma_f32_16x16x32_bf16 v[68:71], v[160:163], v[192:195], v[68:71]
	s_setprio 0
	s_setprio 1
	v_mfma_f32_16x16x32_bf16 v[120:123], v[156:159], v[172:175], v[120:123]
	v_mfma_f32_16x16x32_bf16 v[112:115], v[164:167], v[172:175], v[112:115]
	v_mfma_f32_16x16x32_bf16 v[104:107], v[156:159], v[180:183], v[104:107]
	v_mfma_f32_16x16x32_bf16 v[96:99], v[164:167], v[180:183], v[96:99]
	v_mfma_f32_16x16x32_bf16 v[88:91], v[156:159], v[188:191], v[88:91]
	v_mfma_f32_16x16x32_bf16 v[76:79], v[164:167], v[188:191], v[76:79]
	v_mfma_f32_16x16x32_bf16 v[72:75], v[156:159], v[196:199], v[72:75]
	v_mfma_f32_16x16x32_bf16 v[68:71], v[164:167], v[196:199], v[68:71]
	s_setprio 0
	s_barrier
	s_add_i32 s42, s63, s45
	v_lshl_add_u64 v[224:225], s[40:41], 0, v[210:211]
	s_mov_b32 m0, s42
	ds_read_b128 v[168:171], v244 offset:49152
	ds_read_b128 v[172:175], v244 offset:50176
	ds_read_b128 v[176:179], v244 offset:51200
	ds_read_b128 v[180:183], v244 offset:52224
	ds_read_b128 v[184:187], v244 offset:53248
	ds_read_b128 v[188:191], v244 offset:54272
	ds_read_b128 v[192:195], v244 offset:55296
	ds_read_b128 v[196:199], v244 offset:56320
	global_load_lds_dwordx4 v[224:225], off
	s_add_i32 m0, s42, 0x2000
	s_add_u32 s38, s38, 0xc000
	v_lshl_add_u64 v[224:225], s[40:41], 0, v[208:209]
	s_addc_u32 s39, s39, 0
	s_add_i32 s40, s64, s45
	global_load_lds_dwordx4 v[224:225], off
	v_lshl_add_u64 v[224:225], s[38:39], 0, v[210:211]
	s_mov_b32 m0, s40
	v_lshl_add_u64 v[204:205], v[204:205], 0, s[36:37]
	global_load_lds_dwordx4 v[224:225], off
	v_lshl_add_u64 v[224:225], s[38:39], 0, v[208:209]
	s_add_i32 m0, s40, 0x2000
	s_nop 0
	global_load_lds_dwordx4 v[224:225], off
	s_mov_b32 m0, s55
	s_nop 0
	global_load_lds_dwordx4 v[204:205], off
	v_lshl_add_u64 v[204:205], v[248:249], 0, s[36:37]
	s_mov_b32 m0, s56
	s_nop 0
	global_load_lds_dwordx4 v[204:205], off
	s_waitcnt vmcnt(8)
	s_waitcnt lgkmcnt(0)
	s_barrier
	s_setprio 1
	s_waitcnt lgkmcnt(0)
	v_mfma_f32_16x16x32_bf16 v[64:67], v[136:139], v[168:171], v[64:67]
	v_mfma_f32_16x16x32_bf16 v[60:63], v[144:147], v[168:171], v[60:63]
	v_mfma_f32_16x16x32_bf16 v[56:59], v[136:139], v[176:179], v[56:59]
	v_mfma_f32_16x16x32_bf16 v[48:51], v[144:147], v[176:179], v[48:51]
	v_mfma_f32_16x16x32_bf16 v[40:43], v[136:139], v[184:187], v[40:43]
	v_mfma_f32_16x16x32_bf16 v[32:35], v[144:147], v[184:187], v[32:35]
	v_mfma_f32_16x16x32_bf16 v[24:27], v[136:139], v[192:195], v[24:27]
	v_mfma_f32_16x16x32_bf16 v[16:19], v[144:147], v[192:195], v[16:19]
	s_setprio 0
	s_setprio 1
	v_mfma_f32_16x16x32_bf16 v[64:67], v[140:143], v[172:175], v[64:67]
	v_mfma_f32_16x16x32_bf16 v[60:63], v[148:151], v[172:175], v[60:63]
	v_mfma_f32_16x16x32_bf16 v[56:59], v[140:143], v[180:183], v[56:59]
	v_mfma_f32_16x16x32_bf16 v[48:51], v[148:151], v[180:183], v[48:51]
	v_mfma_f32_16x16x32_bf16 v[40:43], v[140:143], v[188:191], v[40:43]
	v_mfma_f32_16x16x32_bf16 v[32:35], v[148:151], v[188:191], v[32:35]
	v_mfma_f32_16x16x32_bf16 v[24:27], v[140:143], v[196:199], v[24:27]
	v_mfma_f32_16x16x32_bf16 v[16:19], v[148:151], v[196:199], v[16:19]
	s_setprio 0
	s_setprio 1
	v_mfma_f32_16x16x32_bf16 v[52:55], v[152:155], v[168:171], v[52:55]
	v_mfma_f32_16x16x32_bf16 v[44:47], v[160:163], v[168:171], v[44:47]
	v_mfma_f32_16x16x32_bf16 v[36:39], v[152:155], v[176:179], v[36:39]
	v_mfma_f32_16x16x32_bf16 v[28:31], v[160:163], v[176:179], v[28:31]
	v_mfma_f32_16x16x32_bf16 v[20:23], v[152:155], v[184:187], v[20:23]
	v_mfma_f32_16x16x32_bf16 v[12:15], v[160:163], v[184:187], v[12:15]
	v_mfma_f32_16x16x32_bf16 v[8:11], v[152:155], v[192:195], v[8:11]
	v_mfma_f32_16x16x32_bf16 v[4:7], v[160:163], v[192:195], v[4:7]
	s_setprio 0
	s_setprio 1
	v_mfma_f32_16x16x32_bf16 v[52:55], v[156:159], v[172:175], v[52:55]
	v_mfma_f32_16x16x32_bf16 v[44:47], v[164:167], v[172:175], v[44:47]
	v_mfma_f32_16x16x32_bf16 v[36:39], v[156:159], v[180:183], v[36:39]
	v_mfma_f32_16x16x32_bf16 v[28:31], v[164:167], v[180:183], v[28:31]
	v_mfma_f32_16x16x32_bf16 v[20:23], v[156:159], v[188:191], v[20:23]
	v_mfma_f32_16x16x32_bf16 v[12:15], v[164:167], v[188:191], v[12:15]
	v_mfma_f32_16x16x32_bf16 v[8:11], v[156:159], v[196:199], v[8:11]
	v_mfma_f32_16x16x32_bf16 v[4:7], v[164:167], v[196:199], v[4:7]
	s_setprio 0
	s_barrier
	s_add_i32 s62, s62, 2
	s_add_u32 s60, s60, 0x10000
	s_addc_u32 s61, s61, 0
	s_add_u32 s14, s14, 0x100
	s_addc_u32 s15, s15, 0
	s_cmp_gt_u32 s62, 29
	s_cbranch_scc1 .LBB0_147

.LBB0_294:
	s_add_u32 s40, s14, 0x80
	s_addc_u32 s41, s15, 0
	s_waitcnt vmcnt(8)
	s_and_b64 s[38:39], s[38:39], exec
	s_waitcnt lgkmcnt(0)
	s_cselect_b32 s38, s13, s59
	s_cselect_b32 s43, s1, s41
	s_cselect_b32 s42, s0, s40
	s_cselect_b32 s39, s9, s60
	s_add_u32 s40, s38, 0x8000
	s_addc_u32 s41, s39, 0
	s_barrier
	s_setprio 1
	s_waitcnt lgkmcnt(0)
	v_mfma_f32_16x16x32_bf16 v[132:135], v[152:155], v[192:195], v[132:135]
	v_mfma_f32_16x16x32_bf16 v[128:131], v[160:163], v[192:195], v[128:131]
	v_mfma_f32_16x16x32_bf16 v[124:127], v[152:155], v[184:187], v[124:127]
	v_mfma_f32_16x16x32_bf16 v[120:123], v[160:163], v[184:187], v[120:123]
	v_mfma_f32_16x16x32_bf16 v[108:111], v[152:155], v[176:179], v[108:111]
	v_mfma_f32_16x16x32_bf16 v[104:107], v[160:163], v[176:179], v[104:107]
	v_mfma_f32_16x16x32_bf16 v[92:95], v[152:155], v[168:171], v[92:95]
	v_mfma_f32_16x16x32_bf16 v[88:91], v[160:163], v[168:171], v[88:91]
	s_setprio 0
	s_setprio 1
	v_mfma_f32_16x16x32_bf16 v[132:135], v[156:159], v[196:199], v[132:135]
	v_mfma_f32_16x16x32_bf16 v[128:131], v[164:167], v[196:199], v[128:131]
	v_mfma_f32_16x16x32_bf16 v[124:127], v[156:159], v[188:191], v[124:127]
	v_mfma_f32_16x16x32_bf16 v[120:123], v[164:167], v[188:191], v[120:123]
	v_mfma_f32_16x16x32_bf16 v[108:111], v[156:159], v[180:183], v[108:111]
	v_mfma_f32_16x16x32_bf16 v[104:107], v[164:167], v[180:183], v[104:107]
	v_mfma_f32_16x16x32_bf16 v[92:95], v[156:159], v[172:175], v[92:95]
	v_mfma_f32_16x16x32_bf16 v[88:91], v[164:167], v[172:175], v[88:91]
	s_setprio 0
	s_setprio 1
	v_mfma_f32_16x16x32_bf16 v[116:119], v[136:139], v[192:195], v[116:119]
	v_mfma_f32_16x16x32_bf16 v[112:115], v[144:147], v[192:195], v[112:115]
	v_mfma_f32_16x16x32_bf16 v[100:103], v[136:139], v[184:187], v[100:103]
	v_mfma_f32_16x16x32_bf16 v[96:99], v[144:147], v[184:187], v[96:99]
	v_mfma_f32_16x16x32_bf16 v[80:83], v[136:139], v[176:179], v[80:83]
	v_mfma_f32_16x16x32_bf16 v[76:79], v[144:147], v[176:179], v[76:79]
	v_mfma_f32_16x16x32_bf16 v[72:75], v[136:139], v[168:171], v[72:75]
	v_mfma_f32_16x16x32_bf16 v[68:71], v[144:147], v[168:171], v[68:71]
	s_setprio 0
	s_setprio 1
	v_mfma_f32_16x16x32_bf16 v[116:119], v[140:143], v[196:199], v[116:119]
	v_mfma_f32_16x16x32_bf16 v[112:115], v[148:151], v[196:199], v[112:115]
	v_mfma_f32_16x16x32_bf16 v[100:103], v[140:143], v[188:191], v[100:103]
	v_mfma_f32_16x16x32_bf16 v[96:99], v[148:151], v[188:191], v[96:99]
	v_mfma_f32_16x16x32_bf16 v[80:83], v[140:143], v[180:183], v[80:83]
	v_mfma_f32_16x16x32_bf16 v[76:79], v[148:151], v[180:183], v[76:79]
	v_mfma_f32_16x16x32_bf16 v[72:75], v[140:143], v[172:175], v[72:75]
	v_mfma_f32_16x16x32_bf16 v[68:71], v[148:151], v[172:175], v[68:71]
	s_setprio 0
	s_barrier
	s_mov_b32 m0, s47
	v_lshl_add_u64 v[204:205], s[38:39], 0, v[210:211]
	s_add_u32 s62, s38, 0x4000
	ds_read_b128 v[168:171], v244 offset:16384
	ds_read_b128 v[172:175], v244 offset:17408
	ds_read_b128 v[176:179], v244 offset:18432
	ds_read_b128 v[180:183], v244 offset:19456
	ds_read_b128 v[184:187], v244 offset:20480
	ds_read_b128 v[188:191], v244 offset:21504
	ds_read_b128 v[192:195], v244 offset:22528
	ds_read_b128 v[196:199], v244 offset:23552
	global_load_lds_dwordx4 v[204:205], off
	v_lshl_add_u64 v[204:205], s[38:39], 0, v[208:209]
	s_mov_b32 m0, s48
	s_addc_u32 s63, s39, 0
	global_load_lds_dwordx4 v[204:205], off
	v_lshl_add_u64 v[204:205], s[62:63], 0, v[210:211]
	s_mov_b32 m0, s49
	v_mov_b32_e32 v215, v3
	global_load_lds_dwordx4 v[204:205], off
	v_lshl_add_u64 v[204:205], s[62:63], 0, v[208:209]
	s_mov_b32 m0, s50
	v_lshl_add_u64 v[248:249], s[42:43], 0, v[214:215]
	global_load_lds_dwordx4 v[204:205], off
	s_mov_b32 m0, s45
	v_lshl_add_u64 v[204:205], s[42:43], 0, v[2:3]
	global_load_lds_dwordx4 v2, s[42:43]
	s_mov_b32 m0, s51
	s_nop 0
	global_load_lds_dwordx4 v214, s[42:43]
	s_waitcnt vmcnt(8)
	s_waitcnt lgkmcnt(0)
	s_barrier
	s_setprio 1
	s_waitcnt lgkmcnt(0)
	v_mfma_f32_16x16x32_bf16 v[64:67], v[152:155], v[168:171], v[64:67]
	v_mfma_f32_16x16x32_bf16 v[60:63], v[160:163], v[168:171], v[60:63]
	v_mfma_f32_16x16x32_bf16 v[56:59], v[152:155], v[176:179], v[56:59]
	v_mfma_f32_16x16x32_bf16 v[52:55], v[160:163], v[176:179], v[52:55]
	v_mfma_f32_16x16x32_bf16 v[40:43], v[152:155], v[184:187], v[40:43]
	v_mfma_f32_16x16x32_bf16 v[36:39], v[160:163], v[184:187], v[36:39]
	v_mfma_f32_16x16x32_bf16 v[24:27], v[152:155], v[192:195], v[24:27]
	v_mfma_f32_16x16x32_bf16 v[20:23], v[160:163], v[192:195], v[20:23]
	s_setprio 0
	s_setprio 1
	v_mfma_f32_16x16x32_bf16 v[64:67], v[156:159], v[172:175], v[64:67]
	v_mfma_f32_16x16x32_bf16 v[60:63], v[164:167], v[172:175], v[60:63]
	v_mfma_f32_16x16x32_bf16 v[56:59], v[156:159], v[180:183], v[56:59]
	v_mfma_f32_16x16x32_bf16 v[52:55], v[164:167], v[180:183], v[52:55]
	v_mfma_f32_16x16x32_bf16 v[40:43], v[156:159], v[188:191], v[40:43]
	v_mfma_f32_16x16x32_bf16 v[36:39], v[164:167], v[188:191], v[36:39]
	v_mfma_f32_16x16x32_bf16 v[24:27], v[156:159], v[196:199], v[24:27]
	v_mfma_f32_16x16x32_bf16 v[20:23], v[164:167], v[196:199], v[20:23]
	s_setprio 0
	s_setprio 1
	v_mfma_f32_16x16x32_bf16 v[48:51], v[136:139], v[168:171], v[48:51]
	v_mfma_f32_16x16x32_bf16 v[44:47], v[144:147], v[168:171], v[44:47]
	v_mfma_f32_16x16x32_bf16 v[32:35], v[136:139], v[176:179], v[32:35]
	v_mfma_f32_16x16x32_bf16 v[28:31], v[144:147], v[176:179], v[28:31]
	v_mfma_f32_16x16x32_bf16 v[16:19], v[136:139], v[184:187], v[16:19]
	v_mfma_f32_16x16x32_bf16 v[12:15], v[144:147], v[184:187], v[12:15]
	v_mfma_f32_16x16x32_bf16 v[8:11], v[136:139], v[192:195], v[8:11]
	v_mfma_f32_16x16x32_bf16 v[4:7], v[144:147], v[192:195], v[4:7]
	s_setprio 0
	s_setprio 1
	v_mfma_f32_16x16x32_bf16 v[48:51], v[140:143], v[172:175], v[48:51]
	v_mfma_f32_16x16x32_bf16 v[44:47], v[148:151], v[172:175], v[44:47]
	v_mfma_f32_16x16x32_bf16 v[32:35], v[140:143], v[180:183], v[32:35]
	v_mfma_f32_16x16x32_bf16 v[28:31], v[148:151], v[180:183], v[28:31]
	v_mfma_f32_16x16x32_bf16 v[16:19], v[140:143], v[188:191], v[16:19]
	v_mfma_f32_16x16x32_bf16 v[12:15], v[148:151], v[188:191], v[12:15]
	v_mfma_f32_16x16x32_bf16 v[8:11], v[140:143], v[196:199], v[8:11]
	v_mfma_f32_16x16x32_bf16 v[4:7], v[148:151], v[196:199], v[4:7]
	s_setprio 0
	s_barrier
	s_add_i32 s62, 0, 0x18000
	s_add_i32 s63, 0, 0x1c000
	v_add_u32_e32 v148, s62, v243
	v_add_u32_e32 v164, s63, v243
	ds_read_b128 v[136:139], v148
	ds_read_b128 v[140:143], v148 offset:1024
	ds_read_b128 v[144:147], v148 offset:2048
	ds_read_b128 v[148:151], v148 offset:3072
	ds_read_b128 v[152:155], v164
	ds_read_b128 v[156:159], v164 offset:1024
	ds_read_b128 v[160:163], v164 offset:2048
	ds_read_b128 v[164:167], v164 offset:3072
	s_mov_b32 m0, s52
	v_lshl_add_u64 v[226:227], s[42:43], 0, v[226:227]
	ds_read_b128 v[168:171], v244 offset:32768
	ds_read_b128 v[172:175], v244 offset:33792
	ds_read_b128 v[176:179], v244 offset:34816
	ds_read_b128 v[180:183], v244 offset:35840
	ds_read_b128 v[184:187], v244 offset:36864
	ds_read_b128 v[188:191], v244 offset:37888
	ds_read_b128 v[192:195], v244 offset:38912
	ds_read_b128 v[196:199], v244 offset:39936
	global_load_lds_dwordx4 v[226:227], off
	v_lshl_add_u64 v[224:225], s[42:43], 0, v[224:225]
	s_mov_b32 m0, s53
	s_nop 0
	global_load_lds_dwordx4 v[224:225], off
	s_waitcnt vmcnt(8)
	s_waitcnt lgkmcnt(0)
	s_barrier
	s_setprio 1
	s_waitcnt lgkmcnt(0)
	v_mfma_f32_16x16x32_bf16 v[132:135], v[136:139], v[168:171], v[132:135]
	v_mfma_f32_16x16x32_bf16 v[128:131], v[144:147], v[168:171], v[128:131]
	v_mfma_f32_16x16x32_bf16 v[124:127], v[136:139], v[176:179], v[124:127]
	v_mfma_f32_16x16x32_bf16 v[120:123], v[144:147], v[176:179], v[120:123]
	v_mfma_f32_16x16x32_bf16 v[108:111], v[136:139], v[184:187], v[108:111]
	v_mfma_f32_16x16x32_bf16 v[104:107], v[144:147], v[184:187], v[104:107]
	v_mfma_f32_16x16x32_bf16 v[92:95], v[136:139], v[192:195], v[92:95]
	v_mfma_f32_16x16x32_bf16 v[88:91], v[144:147], v[192:195], v[88:91]
	s_setprio 0
	s_setprio 1
	v_mfma_f32_16x16x32_bf16 v[132:135], v[140:143], v[172:175], v[132:135]
	v_mfma_f32_16x16x32_bf16 v[128:131], v[148:151], v[172:175], v[128:131]
	v_mfma_f32_16x16x32_bf16 v[124:127], v[140:143], v[180:183], v[124:127]
	v_mfma_f32_16x16x32_bf16 v[120:123], v[148:151], v[180:183], v[120:123]
	v_mfma_f32_16x16x32_bf16 v[108:111], v[140:143], v[188:191], v[108:111]
	v_mfma_f32_16x16x32_bf16 v[104:107], v[148:151], v[188:191], v[104:107]
	v_mfma_f32_16x16x32_bf16 v[92:95], v[140:143], v[196:199], v[92:95]
	v_mfma_f32_16x16x32_bf16 v[88:91], v[148:151], v[196:199], v[88:91]
	s_setprio 0
	s_setprio 1
	v_mfma_f32_16x16x32_bf16 v[116:119], v[152:155], v[168:171], v[116:119]
	v_mfma_f32_16x16x32_bf16 v[112:115], v[160:163], v[168:171], v[112:115]
	v_mfma_f32_16x16x32_bf16 v[100:103], v[152:155], v[176:179], v[100:103]
	v_mfma_f32_16x16x32_bf16 v[96:99], v[160:163], v[176:179], v[96:99]
	v_mfma_f32_16x16x32_bf16 v[80:83], v[152:155], v[184:187], v[80:83]
	v_mfma_f32_16x16x32_bf16 v[76:79], v[160:163], v[184:187], v[76:79]
	v_mfma_f32_16x16x32_bf16 v[72:75], v[152:155], v[192:195], v[72:75]
	v_mfma_f32_16x16x32_bf16 v[68:71], v[160:163], v[192:195], v[68:71]
	s_setprio 0
	s_setprio 1
	v_mfma_f32_16x16x32_bf16 v[116:119], v[156:159], v[172:175], v[116:119]
	v_mfma_f32_16x16x32_bf16 v[112:115], v[164:167], v[172:175], v[112:115]
	v_mfma_f32_16x16x32_bf16 v[100:103], v[156:159], v[180:183], v[100:103]
	v_mfma_f32_16x16x32_bf16 v[96:99], v[164:167], v[180:183], v[96:99]
	v_mfma_f32_16x16x32_bf16 v[80:83], v[156:159], v[188:191], v[80:83]
	v_mfma_f32_16x16x32_bf16 v[76:79], v[164:167], v[188:191], v[76:79]
	v_mfma_f32_16x16x32_bf16 v[72:75], v[156:159], v[196:199], v[72:75]
	v_mfma_f32_16x16x32_bf16 v[68:71], v[164:167], v[196:199], v[68:71]
	s_setprio 0
	s_barrier
	s_add_i32 s42, s62, s44
	v_lshl_add_u64 v[224:225], s[40:41], 0, v[210:211]
	s_mov_b32 m0, s42
	ds_read_b128 v[168:171], v244 offset:49152
	ds_read_b128 v[172:175], v244 offset:50176
	ds_read_b128 v[176:179], v244 offset:51200
	ds_read_b128 v[180:183], v244 offset:52224
	ds_read_b128 v[184:187], v244 offset:53248
	ds_read_b128 v[188:191], v244 offset:54272
	ds_read_b128 v[192:195], v244 offset:55296
	ds_read_b128 v[196:199], v244 offset:56320
	global_load_lds_dwordx4 v[224:225], off
	s_add_i32 m0, s42, 0x2000
	s_add_u32 s38, s38, 0xc000
	v_lshl_add_u64 v[224:225], s[40:41], 0, v[208:209]
	s_addc_u32 s39, s39, 0
	s_add_i32 s40, s63, s44
	global_load_lds_dwordx4 v[224:225], off
	v_lshl_add_u64 v[224:225], s[38:39], 0, v[210:211]
	s_mov_b32 m0, s40
	v_lshl_add_u64 v[204:205], v[204:205], 0, s[36:37]
	global_load_lds_dwordx4 v[224:225], off
	v_lshl_add_u64 v[224:225], s[38:39], 0, v[208:209]
	s_add_i32 m0, s40, 0x2000
	s_nop 0
	global_load_lds_dwordx4 v[224:225], off
	s_mov_b32 m0, s54
	s_nop 0
	global_load_lds_dwordx4 v[204:205], off
	v_lshl_add_u64 v[204:205], v[248:249], 0, s[36:37]
	s_mov_b32 m0, s55
	s_nop 0
	global_load_lds_dwordx4 v[204:205], off
	s_waitcnt vmcnt(8)
	s_waitcnt lgkmcnt(0)
	s_barrier
	s_setprio 1
	s_waitcnt lgkmcnt(0)
	v_mfma_f32_16x16x32_bf16 v[64:67], v[136:139], v[168:171], v[64:67]
	v_mfma_f32_16x16x32_bf16 v[60:63], v[144:147], v[168:171], v[60:63]
	v_mfma_f32_16x16x32_bf16 v[56:59], v[136:139], v[176:179], v[56:59]
	v_mfma_f32_16x16x32_bf16 v[52:55], v[144:147], v[176:179], v[52:55]
	v_mfma_f32_16x16x32_bf16 v[40:43], v[136:139], v[184:187], v[40:43]
	v_mfma_f32_16x16x32_bf16 v[36:39], v[144:147], v[184:187], v[36:39]
	v_mfma_f32_16x16x32_bf16 v[24:27], v[136:139], v[192:195], v[24:27]
	v_mfma_f32_16x16x32_bf16 v[20:23], v[144:147], v[192:195], v[20:23]
	s_setprio 0
	s_setprio 1
	v_mfma_f32_16x16x32_bf16 v[64:67], v[140:143], v[172:175], v[64:67]
	v_mfma_f32_16x16x32_bf16 v[60:63], v[148:151], v[172:175], v[60:63]
	v_mfma_f32_16x16x32_bf16 v[56:59], v[140:143], v[180:183], v[56:59]
	v_mfma_f32_16x16x32_bf16 v[52:55], v[148:151], v[180:183], v[52:55]
	v_mfma_f32_16x16x32_bf16 v[40:43], v[140:143], v[188:191], v[40:43]
	v_mfma_f32_16x16x32_bf16 v[36:39], v[148:151], v[188:191], v[36:39]
	v_mfma_f32_16x16x32_bf16 v[24:27], v[140:143], v[196:199], v[24:27]
	v_mfma_f32_16x16x32_bf16 v[20:23], v[148:151], v[196:199], v[20:23]
	s_setprio 0
	s_setprio 1
	v_mfma_f32_16x16x32_bf16 v[48:51], v[152:155], v[168:171], v[48:51]
	v_mfma_f32_16x16x32_bf16 v[44:47], v[160:163], v[168:171], v[44:47]
	v_mfma_f32_16x16x32_bf16 v[32:35], v[152:155], v[176:179], v[32:35]
	v_mfma_f32_16x16x32_bf16 v[28:31], v[160:163], v[176:179], v[28:31]
	v_mfma_f32_16x16x32_bf16 v[16:19], v[152:155], v[184:187], v[16:19]
	v_mfma_f32_16x16x32_bf16 v[12:15], v[160:163], v[184:187], v[12:15]
	v_mfma_f32_16x16x32_bf16 v[8:11], v[152:155], v[192:195], v[8:11]
	v_mfma_f32_16x16x32_bf16 v[4:7], v[160:163], v[192:195], v[4:7]
	s_setprio 0
	s_setprio 1
	v_mfma_f32_16x16x32_bf16 v[48:51], v[156:159], v[172:175], v[48:51]
	v_mfma_f32_16x16x32_bf16 v[44:47], v[164:167], v[172:175], v[44:47]
	v_mfma_f32_16x16x32_bf16 v[32:35], v[156:159], v[180:183], v[32:35]
	v_mfma_f32_16x16x32_bf16 v[28:31], v[164:167], v[180:183], v[28:31]
	v_mfma_f32_16x16x32_bf16 v[16:19], v[156:159], v[188:191], v[16:19]
	v_mfma_f32_16x16x32_bf16 v[12:15], v[164:167], v[188:191], v[12:15]
	v_mfma_f32_16x16x32_bf16 v[8:11], v[156:159], v[196:199], v[8:11]
	v_mfma_f32_16x16x32_bf16 v[4:7], v[164:167], v[196:199], v[4:7]
	s_setprio 0
	s_barrier
	s_add_i32 s61, s61, 2
	s_add_u32 s59, s59, 0x10000
	s_addc_u32 s60, s60, 0
	s_add_u32 s14, s14, 0x100
	s_addc_u32 s15, s15, 0
	s_cmp_gt_u32 s61, 29
	s_cbranch_scc1 .LBB0_297

.LBB0_498:
	s_add_u32 s38, s12, 0x80
	s_addc_u32 s39, s13, 0
	s_waitcnt vmcnt(8)
	s_and_b64 s[14:15], s[14:15], exec
	s_waitcnt lgkmcnt(0)
	s_cselect_b32 s14, s60, s61
	s_cselect_b32 s41, s31, s39
	s_cselect_b32 s40, s30, s38
	s_cselect_b32 s15, s9, s62
	s_add_u32 s38, s14, 0x8000
	s_addc_u32 s39, s15, 0
	s_barrier
	s_setprio 1
	s_waitcnt lgkmcnt(0)
	v_mfma_f32_16x16x32_bf16 v[132:135], v[152:155], v[192:195], v[132:135]
	v_mfma_f32_16x16x32_bf16 v[128:131], v[160:163], v[192:195], v[128:131]
	v_mfma_f32_16x16x32_bf16 v[124:127], v[152:155], v[184:187], v[124:127]
	v_mfma_f32_16x16x32_bf16 v[120:123], v[160:163], v[184:187], v[120:123]
	v_mfma_f32_16x16x32_bf16 v[108:111], v[152:155], v[176:179], v[108:111]
	v_mfma_f32_16x16x32_bf16 v[104:107], v[160:163], v[176:179], v[104:107]
	v_mfma_f32_16x16x32_bf16 v[92:95], v[152:155], v[168:171], v[92:95]
	v_mfma_f32_16x16x32_bf16 v[88:91], v[160:163], v[168:171], v[88:91]
	s_setprio 0
	s_setprio 1
	v_mfma_f32_16x16x32_bf16 v[132:135], v[156:159], v[196:199], v[132:135]
	v_mfma_f32_16x16x32_bf16 v[128:131], v[164:167], v[196:199], v[128:131]
	v_mfma_f32_16x16x32_bf16 v[124:127], v[156:159], v[188:191], v[124:127]
	v_mfma_f32_16x16x32_bf16 v[120:123], v[164:167], v[188:191], v[120:123]
	v_mfma_f32_16x16x32_bf16 v[108:111], v[156:159], v[180:183], v[108:111]
	v_mfma_f32_16x16x32_bf16 v[104:107], v[164:167], v[180:183], v[104:107]
	v_mfma_f32_16x16x32_bf16 v[92:95], v[156:159], v[172:175], v[92:95]
	v_mfma_f32_16x16x32_bf16 v[88:91], v[164:167], v[172:175], v[88:91]
	s_setprio 0
	s_setprio 1
	v_mfma_f32_16x16x32_bf16 v[116:119], v[136:139], v[192:195], v[116:119]
	v_mfma_f32_16x16x32_bf16 v[112:115], v[144:147], v[192:195], v[112:115]
	v_mfma_f32_16x16x32_bf16 v[100:103], v[136:139], v[184:187], v[100:103]
	v_mfma_f32_16x16x32_bf16 v[96:99], v[144:147], v[184:187], v[96:99]
	v_mfma_f32_16x16x32_bf16 v[80:83], v[136:139], v[176:179], v[80:83]
	v_mfma_f32_16x16x32_bf16 v[76:79], v[144:147], v[176:179], v[76:79]
	v_mfma_f32_16x16x32_bf16 v[72:75], v[136:139], v[168:171], v[72:75]
	v_mfma_f32_16x16x32_bf16 v[68:71], v[144:147], v[168:171], v[68:71]
	s_setprio 0
	s_setprio 1
	v_mfma_f32_16x16x32_bf16 v[116:119], v[140:143], v[196:199], v[116:119]
	v_mfma_f32_16x16x32_bf16 v[112:115], v[148:151], v[196:199], v[112:115]
	v_mfma_f32_16x16x32_bf16 v[100:103], v[140:143], v[188:191], v[100:103]
	v_mfma_f32_16x16x32_bf16 v[96:99], v[148:151], v[188:191], v[96:99]
	v_mfma_f32_16x16x32_bf16 v[80:83], v[140:143], v[180:183], v[80:83]
	v_mfma_f32_16x16x32_bf16 v[76:79], v[148:151], v[180:183], v[76:79]
	v_mfma_f32_16x16x32_bf16 v[72:75], v[140:143], v[172:175], v[72:75]
	v_mfma_f32_16x16x32_bf16 v[68:71], v[148:151], v[172:175], v[68:71]
	s_setprio 0
	s_barrier
	s_mov_b32 m0, s44
	v_lshl_add_u64 v[246:247], s[14:15], 0, v[210:211]
	s_add_u32 s64, s14, 0x4000
	ds_read_b128 v[168:171], v243 offset:16384
	ds_read_b128 v[172:175], v243 offset:17408
	ds_read_b128 v[176:179], v243 offset:18432
	ds_read_b128 v[180:183], v243 offset:19456
	ds_read_b128 v[184:187], v243 offset:20480
	ds_read_b128 v[188:191], v243 offset:21504
	ds_read_b128 v[192:195], v243 offset:22528
	ds_read_b128 v[196:199], v243 offset:23552
	global_load_lds_dwordx4 v[246:247], off
	v_lshl_add_u64 v[246:247], s[14:15], 0, v[208:209]
	s_mov_b32 m0, s45
	s_addc_u32 s65, s15, 0
	global_load_lds_dwordx4 v[246:247], off
	v_lshl_add_u64 v[246:247], s[64:65], 0, v[210:211]
	s_mov_b32 m0, s47
	v_mov_b32_e32 v215, v3
	global_load_lds_dwordx4 v[246:247], off
	v_lshl_add_u64 v[246:247], s[64:65], 0, v[208:209]
	s_mov_b32 m0, s48
	v_lshl_add_u64 v[248:249], s[40:41], 0, v[214:215]
	global_load_lds_dwordx4 v[246:247], off
	s_mov_b32 m0, s43
	v_lshl_add_u64 v[246:247], s[40:41], 0, v[2:3]
	global_load_lds_dwordx4 v2, s[40:41]
	s_mov_b32 m0, s49
	s_nop 0
	global_load_lds_dwordx4 v214, s[40:41]
	s_waitcnt vmcnt(8)
	s_waitcnt lgkmcnt(0)
	s_barrier
	s_setprio 1
	s_waitcnt lgkmcnt(0)
	v_mfma_f32_16x16x32_bf16 v[64:67], v[152:155], v[168:171], v[64:67]
	v_mfma_f32_16x16x32_bf16 v[60:63], v[160:163], v[168:171], v[60:63]
	v_mfma_f32_16x16x32_bf16 v[56:59], v[152:155], v[176:179], v[56:59]
	v_mfma_f32_16x16x32_bf16 v[52:55], v[160:163], v[176:179], v[52:55]
	v_mfma_f32_16x16x32_bf16 v[40:43], v[152:155], v[184:187], v[40:43]
	v_mfma_f32_16x16x32_bf16 v[36:39], v[160:163], v[184:187], v[36:39]
	v_mfma_f32_16x16x32_bf16 v[24:27], v[152:155], v[192:195], v[24:27]
	v_mfma_f32_16x16x32_bf16 v[20:23], v[160:163], v[192:195], v[20:23]
	s_setprio 0
	s_setprio 1
	v_mfma_f32_16x16x32_bf16 v[64:67], v[156:159], v[172:175], v[64:67]
	v_mfma_f32_16x16x32_bf16 v[60:63], v[164:167], v[172:175], v[60:63]
	v_mfma_f32_16x16x32_bf16 v[56:59], v[156:159], v[180:183], v[56:59]
	v_mfma_f32_16x16x32_bf16 v[52:55], v[164:167], v[180:183], v[52:55]
	v_mfma_f32_16x16x32_bf16 v[40:43], v[156:159], v[188:191], v[40:43]
	v_mfma_f32_16x16x32_bf16 v[36:39], v[164:167], v[188:191], v[36:39]
	v_mfma_f32_16x16x32_bf16 v[24:27], v[156:159], v[196:199], v[24:27]
	v_mfma_f32_16x16x32_bf16 v[20:23], v[164:167], v[196:199], v[20:23]
	s_setprio 0
	s_setprio 1
	v_mfma_f32_16x16x32_bf16 v[48:51], v[136:139], v[168:171], v[48:51]
	v_mfma_f32_16x16x32_bf16 v[44:47], v[144:147], v[168:171], v[44:47]
	v_mfma_f32_16x16x32_bf16 v[32:35], v[136:139], v[176:179], v[32:35]
	v_mfma_f32_16x16x32_bf16 v[28:31], v[144:147], v[176:179], v[28:31]
	v_mfma_f32_16x16x32_bf16 v[16:19], v[136:139], v[184:187], v[16:19]
	v_mfma_f32_16x16x32_bf16 v[12:15], v[144:147], v[184:187], v[12:15]
	v_mfma_f32_16x16x32_bf16 v[8:11], v[136:139], v[192:195], v[8:11]
	v_mfma_f32_16x16x32_bf16 v[4:7], v[144:147], v[192:195], v[4:7]
	s_setprio 0
	s_setprio 1
	v_mfma_f32_16x16x32_bf16 v[48:51], v[140:143], v[172:175], v[48:51]
	v_mfma_f32_16x16x32_bf16 v[44:47], v[148:151], v[172:175], v[44:47]
	v_mfma_f32_16x16x32_bf16 v[32:35], v[140:143], v[180:183], v[32:35]
	v_mfma_f32_16x16x32_bf16 v[28:31], v[148:151], v[180:183], v[28:31]
	v_mfma_f32_16x16x32_bf16 v[16:19], v[140:143], v[188:191], v[16:19]
	v_mfma_f32_16x16x32_bf16 v[12:15], v[148:151], v[188:191], v[12:15]
	v_mfma_f32_16x16x32_bf16 v[8:11], v[140:143], v[196:199], v[8:11]
	v_mfma_f32_16x16x32_bf16 v[4:7], v[148:151], v[196:199], v[4:7]
	s_setprio 0
	s_barrier
	s_add_i32 s64, 0, 0x18000
	s_add_i32 s65, 0, 0x1c000
	v_add_u32_e32 v148, s64, v241
	v_add_u32_e32 v164, s65, v241
	ds_read_b128 v[136:139], v148
	ds_read_b128 v[140:143], v148 offset:1024
	ds_read_b128 v[144:147], v148 offset:2048
	ds_read_b128 v[148:151], v148 offset:3072
	ds_read_b128 v[152:155], v164
	ds_read_b128 v[156:159], v164 offset:1024
	ds_read_b128 v[160:163], v164 offset:2048
	ds_read_b128 v[164:167], v164 offset:3072
	s_mov_b32 m0, s50
	v_lshl_add_u64 v[224:225], s[40:41], 0, v[224:225]
	ds_read_b128 v[168:171], v243 offset:32768
	ds_read_b128 v[172:175], v243 offset:33792
	ds_read_b128 v[176:179], v243 offset:34816
	ds_read_b128 v[180:183], v243 offset:35840
	ds_read_b128 v[184:187], v243 offset:36864
	ds_read_b128 v[188:191], v243 offset:37888
	ds_read_b128 v[192:195], v243 offset:38912
	ds_read_b128 v[196:199], v243 offset:39936
	global_load_lds_dwordx4 v[224:225], off
	v_lshl_add_u64 v[222:223], s[40:41], 0, v[222:223]
	s_mov_b32 m0, s51
	s_nop 0
	global_load_lds_dwordx4 v[222:223], off
	s_waitcnt vmcnt(8)
	s_waitcnt lgkmcnt(0)
	s_barrier
	s_setprio 1
	s_waitcnt lgkmcnt(0)
	v_mfma_f32_16x16x32_bf16 v[132:135], v[136:139], v[168:171], v[132:135]
	v_mfma_f32_16x16x32_bf16 v[128:131], v[144:147], v[168:171], v[128:131]
	v_mfma_f32_16x16x32_bf16 v[124:127], v[136:139], v[176:179], v[124:127]
	v_mfma_f32_16x16x32_bf16 v[120:123], v[144:147], v[176:179], v[120:123]
	v_mfma_f32_16x16x32_bf16 v[108:111], v[136:139], v[184:187], v[108:111]
	v_mfma_f32_16x16x32_bf16 v[104:107], v[144:147], v[184:187], v[104:107]
	v_mfma_f32_16x16x32_bf16 v[92:95], v[136:139], v[192:195], v[92:95]
	v_mfma_f32_16x16x32_bf16 v[88:91], v[144:147], v[192:195], v[88:91]
	s_setprio 0
	s_setprio 1
	v_mfma_f32_16x16x32_bf16 v[132:135], v[140:143], v[172:175], v[132:135]
	v_mfma_f32_16x16x32_bf16 v[128:131], v[148:151], v[172:175], v[128:131]
	v_mfma_f32_16x16x32_bf16 v[124:127], v[140:143], v[180:183], v[124:127]
	v_mfma_f32_16x16x32_bf16 v[120:123], v[148:151], v[180:183], v[120:123]
	v_mfma_f32_16x16x32_bf16 v[108:111], v[140:143], v[188:191], v[108:111]
	v_mfma_f32_16x16x32_bf16 v[104:107], v[148:151], v[188:191], v[104:107]
	v_mfma_f32_16x16x32_bf16 v[92:95], v[140:143], v[196:199], v[92:95]
	v_mfma_f32_16x16x32_bf16 v[88:91], v[148:151], v[196:199], v[88:91]
	s_setprio 0
	s_setprio 1
	v_mfma_f32_16x16x32_bf16 v[116:119], v[152:155], v[168:171], v[116:119]
	v_mfma_f32_16x16x32_bf16 v[112:115], v[160:163], v[168:171], v[112:115]
	v_mfma_f32_16x16x32_bf16 v[100:103], v[152:155], v[176:179], v[100:103]
	v_mfma_f32_16x16x32_bf16 v[96:99], v[160:163], v[176:179], v[96:99]
	v_mfma_f32_16x16x32_bf16 v[80:83], v[152:155], v[184:187], v[80:83]
	v_mfma_f32_16x16x32_bf16 v[76:79], v[160:163], v[184:187], v[76:79]
	v_mfma_f32_16x16x32_bf16 v[72:75], v[152:155], v[192:195], v[72:75]
	v_mfma_f32_16x16x32_bf16 v[68:71], v[160:163], v[192:195], v[68:71]
	s_setprio 0
	s_setprio 1
	v_mfma_f32_16x16x32_bf16 v[116:119], v[156:159], v[172:175], v[116:119]
	v_mfma_f32_16x16x32_bf16 v[112:115], v[164:167], v[172:175], v[112:115]
	v_mfma_f32_16x16x32_bf16 v[100:103], v[156:159], v[180:183], v[100:103]
	v_mfma_f32_16x16x32_bf16 v[96:99], v[164:167], v[180:183], v[96:99]
	v_mfma_f32_16x16x32_bf16 v[80:83], v[156:159], v[188:191], v[80:83]
	v_mfma_f32_16x16x32_bf16 v[76:79], v[164:167], v[188:191], v[76:79]
	v_mfma_f32_16x16x32_bf16 v[72:75], v[156:159], v[196:199], v[72:75]
	v_mfma_f32_16x16x32_bf16 v[68:71], v[164:167], v[196:199], v[68:71]
	s_setprio 0
	s_barrier
	s_add_i32 s40, s64, s42
	v_lshl_add_u64 v[222:223], s[38:39], 0, v[210:211]
	s_mov_b32 m0, s40
	ds_read_b128 v[168:171], v243 offset:49152
	ds_read_b128 v[172:175], v243 offset:50176
	ds_read_b128 v[176:179], v243 offset:51200
	ds_read_b128 v[180:183], v243 offset:52224
	ds_read_b128 v[184:187], v243 offset:53248
	ds_read_b128 v[188:191], v243 offset:54272
	ds_read_b128 v[192:195], v243 offset:55296
	ds_read_b128 v[196:199], v243 offset:56320
	global_load_lds_dwordx4 v[222:223], off
	s_add_i32 m0, s40, 0x2000
	s_add_u32 s14, s14, 0xc000
	v_lshl_add_u64 v[222:223], s[38:39], 0, v[208:209]
	s_addc_u32 s15, s15, 0
	s_add_i32 s38, s65, s42
	global_load_lds_dwordx4 v[222:223], off
	v_lshl_add_u64 v[222:223], s[14:15], 0, v[210:211]
	s_mov_b32 m0, s38
	s_nop 0
	global_load_lds_dwordx4 v[222:223], off
	v_lshl_add_u64 v[222:223], s[14:15], 0, v[208:209]
	s_add_i32 m0, s38, 0x2000
	s_nop 0
	global_load_lds_dwordx4 v[222:223], off
	v_lshl_add_u64 v[222:223], v[246:247], 0, s[36:37]
	s_mov_b32 m0, s53
	s_nop 0
	global_load_lds_dwordx4 v[222:223], off
	v_lshl_add_u64 v[222:223], v[248:249], 0, s[36:37]
	s_mov_b32 m0, s54
	s_nop 0
	global_load_lds_dwordx4 v[222:223], off
	s_waitcnt vmcnt(8)
	s_waitcnt lgkmcnt(0)
	s_barrier
	s_setprio 1
	s_waitcnt lgkmcnt(0)
	v_mfma_f32_16x16x32_bf16 v[64:67], v[136:139], v[168:171], v[64:67]
	v_mfma_f32_16x16x32_bf16 v[60:63], v[144:147], v[168:171], v[60:63]
	v_mfma_f32_16x16x32_bf16 v[56:59], v[136:139], v[176:179], v[56:59]
	v_mfma_f32_16x16x32_bf16 v[52:55], v[144:147], v[176:179], v[52:55]
	v_mfma_f32_16x16x32_bf16 v[40:43], v[136:139], v[184:187], v[40:43]
	v_mfma_f32_16x16x32_bf16 v[36:39], v[144:147], v[184:187], v[36:39]
	v_mfma_f32_16x16x32_bf16 v[24:27], v[136:139], v[192:195], v[24:27]
	v_mfma_f32_16x16x32_bf16 v[20:23], v[144:147], v[192:195], v[20:23]
	s_setprio 0
	s_setprio 1
	v_mfma_f32_16x16x32_bf16 v[64:67], v[140:143], v[172:175], v[64:67]
	v_mfma_f32_16x16x32_bf16 v[60:63], v[148:151], v[172:175], v[60:63]
	v_mfma_f32_16x16x32_bf16 v[56:59], v[140:143], v[180:183], v[56:59]
	v_mfma_f32_16x16x32_bf16 v[52:55], v[148:151], v[180:183], v[52:55]
	v_mfma_f32_16x16x32_bf16 v[40:43], v[140:143], v[188:191], v[40:43]
	v_mfma_f32_16x16x32_bf16 v[36:39], v[148:151], v[188:191], v[36:39]
	v_mfma_f32_16x16x32_bf16 v[24:27], v[140:143], v[196:199], v[24:27]
	v_mfma_f32_16x16x32_bf16 v[20:23], v[148:151], v[196:199], v[20:23]
	s_setprio 0
	s_setprio 1
	v_mfma_f32_16x16x32_bf16 v[48:51], v[152:155], v[168:171], v[48:51]
	v_mfma_f32_16x16x32_bf16 v[44:47], v[160:163], v[168:171], v[44:47]
	v_mfma_f32_16x16x32_bf16 v[32:35], v[152:155], v[176:179], v[32:35]
	v_mfma_f32_16x16x32_bf16 v[28:31], v[160:163], v[176:179], v[28:31]
	v_mfma_f32_16x16x32_bf16 v[16:19], v[152:155], v[184:187], v[16:19]
	v_mfma_f32_16x16x32_bf16 v[12:15], v[160:163], v[184:187], v[12:15]
	v_mfma_f32_16x16x32_bf16 v[8:11], v[152:155], v[192:195], v[8:11]
	v_mfma_f32_16x16x32_bf16 v[4:7], v[160:163], v[192:195], v[4:7]
	s_setprio 0
	s_setprio 1
	v_mfma_f32_16x16x32_bf16 v[48:51], v[156:159], v[172:175], v[48:51]
	v_mfma_f32_16x16x32_bf16 v[44:47], v[164:167], v[172:175], v[44:47]
	v_mfma_f32_16x16x32_bf16 v[32:35], v[156:159], v[180:183], v[32:35]
	v_mfma_f32_16x16x32_bf16 v[28:31], v[164:167], v[180:183], v[28:31]
	v_mfma_f32_16x16x32_bf16 v[16:19], v[156:159], v[188:191], v[16:19]
	v_mfma_f32_16x16x32_bf16 v[12:15], v[164:167], v[188:191], v[12:15]
	v_mfma_f32_16x16x32_bf16 v[8:11], v[156:159], v[196:199], v[8:11]
	v_mfma_f32_16x16x32_bf16 v[4:7], v[164:167], v[196:199], v[4:7]
	s_setprio 0
	s_barrier
	s_add_i32 s63, s63, 2
	s_add_u32 s61, s61, 0x10000
	s_addc_u32 s62, s62, 0
	s_add_u32 s12, s12, 0x100
	s_addc_u32 s13, s13, 0
	s_cmp_gt_u32 s63, 29
	s_cbranch_scc1 .LBB0_501

.LBB0_835:
	s_add_u32 s40, s14, 0x80
	s_addc_u32 s41, s15, 0
	s_waitcnt vmcnt(8)
	s_and_b64 s[38:39], s[38:39], exec
	s_waitcnt lgkmcnt(0)
	s_cselect_b32 s38, s13, s59
	s_cselect_b32 s43, s1, s41
	s_cselect_b32 s42, s0, s40
	s_cselect_b32 s39, s9, s60
	s_add_u32 s40, s38, 0x8000
	s_addc_u32 s41, s39, 0
	s_barrier
	s_setprio 1
	s_waitcnt lgkmcnt(0)
	v_mfma_f32_16x16x32_bf16 v[132:135], v[152:155], v[192:195], v[132:135]
	v_mfma_f32_16x16x32_bf16 v[128:131], v[160:163], v[192:195], v[128:131]
	v_mfma_f32_16x16x32_bf16 v[124:127], v[152:155], v[184:187], v[124:127]
	v_mfma_f32_16x16x32_bf16 v[120:123], v[160:163], v[184:187], v[120:123]
	v_mfma_f32_16x16x32_bf16 v[108:111], v[152:155], v[176:179], v[108:111]
	v_mfma_f32_16x16x32_bf16 v[104:107], v[160:163], v[176:179], v[104:107]
	v_mfma_f32_16x16x32_bf16 v[92:95], v[152:155], v[168:171], v[92:95]
	v_mfma_f32_16x16x32_bf16 v[88:91], v[160:163], v[168:171], v[88:91]
	s_setprio 0
	s_setprio 1
	v_mfma_f32_16x16x32_bf16 v[132:135], v[156:159], v[196:199], v[132:135]
	v_mfma_f32_16x16x32_bf16 v[128:131], v[164:167], v[196:199], v[128:131]
	v_mfma_f32_16x16x32_bf16 v[124:127], v[156:159], v[188:191], v[124:127]
	v_mfma_f32_16x16x32_bf16 v[120:123], v[164:167], v[188:191], v[120:123]
	v_mfma_f32_16x16x32_bf16 v[108:111], v[156:159], v[180:183], v[108:111]
	v_mfma_f32_16x16x32_bf16 v[104:107], v[164:167], v[180:183], v[104:107]
	v_mfma_f32_16x16x32_bf16 v[92:95], v[156:159], v[172:175], v[92:95]
	v_mfma_f32_16x16x32_bf16 v[88:91], v[164:167], v[172:175], v[88:91]
	s_setprio 0
	s_setprio 1
	v_mfma_f32_16x16x32_bf16 v[116:119], v[136:139], v[192:195], v[116:119]
	v_mfma_f32_16x16x32_bf16 v[112:115], v[144:147], v[192:195], v[112:115]
	v_mfma_f32_16x16x32_bf16 v[100:103], v[136:139], v[184:187], v[100:103]
	v_mfma_f32_16x16x32_bf16 v[96:99], v[144:147], v[184:187], v[96:99]
	v_mfma_f32_16x16x32_bf16 v[80:83], v[136:139], v[176:179], v[80:83]
	v_mfma_f32_16x16x32_bf16 v[76:79], v[144:147], v[176:179], v[76:79]
	v_mfma_f32_16x16x32_bf16 v[72:75], v[136:139], v[168:171], v[72:75]
	v_mfma_f32_16x16x32_bf16 v[68:71], v[144:147], v[168:171], v[68:71]
	s_setprio 0
	s_setprio 1
	v_mfma_f32_16x16x32_bf16 v[116:119], v[140:143], v[196:199], v[116:119]
	v_mfma_f32_16x16x32_bf16 v[112:115], v[148:151], v[196:199], v[112:115]
	v_mfma_f32_16x16x32_bf16 v[100:103], v[140:143], v[188:191], v[100:103]
	v_mfma_f32_16x16x32_bf16 v[96:99], v[148:151], v[188:191], v[96:99]
	v_mfma_f32_16x16x32_bf16 v[80:83], v[140:143], v[180:183], v[80:83]
	v_mfma_f32_16x16x32_bf16 v[76:79], v[148:151], v[180:183], v[76:79]
	v_mfma_f32_16x16x32_bf16 v[72:75], v[140:143], v[172:175], v[72:75]
	v_mfma_f32_16x16x32_bf16 v[68:71], v[148:151], v[172:175], v[68:71]
	s_setprio 0
	s_barrier
	s_mov_b32 m0, s47
	v_lshl_add_u64 v[248:249], s[38:39], 0, v[210:211]
	s_add_u32 s62, s38, 0x4000
	ds_read_b128 v[168:171], v244 offset:16384
	ds_read_b128 v[172:175], v244 offset:17408
	ds_read_b128 v[176:179], v244 offset:18432
	ds_read_b128 v[180:183], v244 offset:19456
	ds_read_b128 v[184:187], v244 offset:20480
	ds_read_b128 v[188:191], v244 offset:21504
	ds_read_b128 v[192:195], v244 offset:22528
	ds_read_b128 v[196:199], v244 offset:23552
	global_load_lds_dwordx4 v[248:249], off
	v_lshl_add_u64 v[248:249], s[38:39], 0, v[208:209]
	s_mov_b32 m0, s48
	s_addc_u32 s63, s39, 0
	global_load_lds_dwordx4 v[248:249], off
	v_lshl_add_u64 v[248:249], s[62:63], 0, v[210:211]
	s_mov_b32 m0, s49
	v_mov_b32_e32 v215, v3
	global_load_lds_dwordx4 v[248:249], off
	v_lshl_add_u64 v[248:249], s[62:63], 0, v[208:209]
	s_mov_b32 m0, s50
	v_lshl_add_u64 v[204:205], s[42:43], 0, v[214:215]
	global_load_lds_dwordx4 v[248:249], off
	s_mov_b32 m0, s45
	v_lshl_add_u64 v[248:249], s[42:43], 0, v[2:3]
	global_load_lds_dwordx4 v2, s[42:43]
	s_mov_b32 m0, s51
	s_nop 0
	global_load_lds_dwordx4 v214, s[42:43]
	s_waitcnt vmcnt(8)
	s_waitcnt lgkmcnt(0)
	s_barrier
	s_setprio 1
	s_waitcnt lgkmcnt(0)
	v_mfma_f32_16x16x32_bf16 v[64:67], v[152:155], v[168:171], v[64:67]
	v_mfma_f32_16x16x32_bf16 v[60:63], v[160:163], v[168:171], v[60:63]
	v_mfma_f32_16x16x32_bf16 v[56:59], v[152:155], v[176:179], v[56:59]
	v_mfma_f32_16x16x32_bf16 v[52:55], v[160:163], v[176:179], v[52:55]
	v_mfma_f32_16x16x32_bf16 v[40:43], v[152:155], v[184:187], v[40:43]
	v_mfma_f32_16x16x32_bf16 v[36:39], v[160:163], v[184:187], v[36:39]
	v_mfma_f32_16x16x32_bf16 v[24:27], v[152:155], v[192:195], v[24:27]
	v_mfma_f32_16x16x32_bf16 v[20:23], v[160:163], v[192:195], v[20:23]
	s_setprio 0
	s_setprio 1
	v_mfma_f32_16x16x32_bf16 v[64:67], v[156:159], v[172:175], v[64:67]
	v_mfma_f32_16x16x32_bf16 v[60:63], v[164:167], v[172:175], v[60:63]
	v_mfma_f32_16x16x32_bf16 v[56:59], v[156:159], v[180:183], v[56:59]
	v_mfma_f32_16x16x32_bf16 v[52:55], v[164:167], v[180:183], v[52:55]
	v_mfma_f32_16x16x32_bf16 v[40:43], v[156:159], v[188:191], v[40:43]
	v_mfma_f32_16x16x32_bf16 v[36:39], v[164:167], v[188:191], v[36:39]
	v_mfma_f32_16x16x32_bf16 v[24:27], v[156:159], v[196:199], v[24:27]
	v_mfma_f32_16x16x32_bf16 v[20:23], v[164:167], v[196:199], v[20:23]
	s_setprio 0
	s_setprio 1
	v_mfma_f32_16x16x32_bf16 v[48:51], v[136:139], v[168:171], v[48:51]
	v_mfma_f32_16x16x32_bf16 v[44:47], v[144:147], v[168:171], v[44:47]
	v_mfma_f32_16x16x32_bf16 v[32:35], v[136:139], v[176:179], v[32:35]
	v_mfma_f32_16x16x32_bf16 v[28:31], v[144:147], v[176:179], v[28:31]
	v_mfma_f32_16x16x32_bf16 v[16:19], v[136:139], v[184:187], v[16:19]
	v_mfma_f32_16x16x32_bf16 v[12:15], v[144:147], v[184:187], v[12:15]
	v_mfma_f32_16x16x32_bf16 v[8:11], v[136:139], v[192:195], v[8:11]
	v_mfma_f32_16x16x32_bf16 v[4:7], v[144:147], v[192:195], v[4:7]
	s_setprio 0
	s_setprio 1
	v_mfma_f32_16x16x32_bf16 v[48:51], v[140:143], v[172:175], v[48:51]
	v_mfma_f32_16x16x32_bf16 v[44:47], v[148:151], v[172:175], v[44:47]
	v_mfma_f32_16x16x32_bf16 v[32:35], v[140:143], v[180:183], v[32:35]
	v_mfma_f32_16x16x32_bf16 v[28:31], v[148:151], v[180:183], v[28:31]
	v_mfma_f32_16x16x32_bf16 v[16:19], v[140:143], v[188:191], v[16:19]
	v_mfma_f32_16x16x32_bf16 v[12:15], v[148:151], v[188:191], v[12:15]
	v_mfma_f32_16x16x32_bf16 v[8:11], v[140:143], v[196:199], v[8:11]
	v_mfma_f32_16x16x32_bf16 v[4:7], v[148:151], v[196:199], v[4:7]
	s_setprio 0
	s_barrier
	s_add_i32 s62, 0, 0x18000
	s_add_i32 s63, 0, 0x1c000
	v_add_u32_e32 v148, s62, v243
	v_add_u32_e32 v164, s63, v243
	ds_read_b128 v[136:139], v148
	ds_read_b128 v[140:143], v148 offset:1024
	ds_read_b128 v[144:147], v148 offset:2048
	ds_read_b128 v[148:151], v148 offset:3072
	ds_read_b128 v[152:155], v164
	ds_read_b128 v[156:159], v164 offset:1024
	ds_read_b128 v[160:163], v164 offset:2048
	ds_read_b128 v[164:167], v164 offset:3072
	s_mov_b32 m0, s52
	v_lshl_add_u64 v[226:227], s[42:43], 0, v[226:227]
	ds_read_b128 v[168:171], v244 offset:32768
	ds_read_b128 v[172:175], v244 offset:33792
	ds_read_b128 v[176:179], v244 offset:34816
	ds_read_b128 v[180:183], v244 offset:35840
	ds_read_b128 v[184:187], v244 offset:36864
	ds_read_b128 v[188:191], v244 offset:37888
	ds_read_b128 v[192:195], v244 offset:38912
	ds_read_b128 v[196:199], v244 offset:39936
	global_load_lds_dwordx4 v[226:227], off
	v_lshl_add_u64 v[224:225], s[42:43], 0, v[224:225]
	s_mov_b32 m0, s53
	s_nop 0
	global_load_lds_dwordx4 v[224:225], off
	s_waitcnt vmcnt(8)
	s_waitcnt lgkmcnt(0)
	s_barrier
	s_setprio 1
	s_waitcnt lgkmcnt(0)
	v_mfma_f32_16x16x32_bf16 v[132:135], v[136:139], v[168:171], v[132:135]
	v_mfma_f32_16x16x32_bf16 v[128:131], v[144:147], v[168:171], v[128:131]
	v_mfma_f32_16x16x32_bf16 v[124:127], v[136:139], v[176:179], v[124:127]
	v_mfma_f32_16x16x32_bf16 v[120:123], v[144:147], v[176:179], v[120:123]
	v_mfma_f32_16x16x32_bf16 v[108:111], v[136:139], v[184:187], v[108:111]
	v_mfma_f32_16x16x32_bf16 v[104:107], v[144:147], v[184:187], v[104:107]
	v_mfma_f32_16x16x32_bf16 v[92:95], v[136:139], v[192:195], v[92:95]
	v_mfma_f32_16x16x32_bf16 v[88:91], v[144:147], v[192:195], v[88:91]
	s_setprio 0
	s_setprio 1
	v_mfma_f32_16x16x32_bf16 v[132:135], v[140:143], v[172:175], v[132:135]
	v_mfma_f32_16x16x32_bf16 v[128:131], v[148:151], v[172:175], v[128:131]
	v_mfma_f32_16x16x32_bf16 v[124:127], v[140:143], v[180:183], v[124:127]
	v_mfma_f32_16x16x32_bf16 v[120:123], v[148:151], v[180:183], v[120:123]
	v_mfma_f32_16x16x32_bf16 v[108:111], v[140:143], v[188:191], v[108:111]
	v_mfma_f32_16x16x32_bf16 v[104:107], v[148:151], v[188:191], v[104:107]
	v_mfma_f32_16x16x32_bf16 v[92:95], v[140:143], v[196:199], v[92:95]
	v_mfma_f32_16x16x32_bf16 v[88:91], v[148:151], v[196:199], v[88:91]
	s_setprio 0
	s_setprio 1
	v_mfma_f32_16x16x32_bf16 v[116:119], v[152:155], v[168:171], v[116:119]
	v_mfma_f32_16x16x32_bf16 v[112:115], v[160:163], v[168:171], v[112:115]
	v_mfma_f32_16x16x32_bf16 v[100:103], v[152:155], v[176:179], v[100:103]
	v_mfma_f32_16x16x32_bf16 v[96:99], v[160:163], v[176:179], v[96:99]
	v_mfma_f32_16x16x32_bf16 v[80:83], v[152:155], v[184:187], v[80:83]
	v_mfma_f32_16x16x32_bf16 v[76:79], v[160:163], v[184:187], v[76:79]
	v_mfma_f32_16x16x32_bf16 v[72:75], v[152:155], v[192:195], v[72:75]
	v_mfma_f32_16x16x32_bf16 v[68:71], v[160:163], v[192:195], v[68:71]
	s_setprio 0
	s_setprio 1
	v_mfma_f32_16x16x32_bf16 v[116:119], v[156:159], v[172:175], v[116:119]
	v_mfma_f32_16x16x32_bf16 v[112:115], v[164:167], v[172:175], v[112:115]
	v_mfma_f32_16x16x32_bf16 v[100:103], v[156:159], v[180:183], v[100:103]
	v_mfma_f32_16x16x32_bf16 v[96:99], v[164:167], v[180:183], v[96:99]
	v_mfma_f32_16x16x32_bf16 v[80:83], v[156:159], v[188:191], v[80:83]
	v_mfma_f32_16x16x32_bf16 v[76:79], v[164:167], v[188:191], v[76:79]
	v_mfma_f32_16x16x32_bf16 v[72:75], v[156:159], v[196:199], v[72:75]
	v_mfma_f32_16x16x32_bf16 v[68:71], v[164:167], v[196:199], v[68:71]
	s_setprio 0
	s_barrier
	s_add_i32 s42, s62, s44
	v_lshl_add_u64 v[224:225], s[40:41], 0, v[210:211]
	s_mov_b32 m0, s42
	ds_read_b128 v[168:171], v244 offset:49152
	ds_read_b128 v[172:175], v244 offset:50176
	ds_read_b128 v[176:179], v244 offset:51200
	ds_read_b128 v[180:183], v244 offset:52224
	ds_read_b128 v[184:187], v244 offset:53248
	ds_read_b128 v[188:191], v244 offset:54272
	ds_read_b128 v[192:195], v244 offset:55296
	ds_read_b128 v[196:199], v244 offset:56320
	global_load_lds_dwordx4 v[224:225], off
	s_add_i32 m0, s42, 0x2000
	s_add_u32 s38, s38, 0xc000
	v_lshl_add_u64 v[224:225], s[40:41], 0, v[208:209]
	s_addc_u32 s39, s39, 0
	s_add_i32 s40, s63, s44
	global_load_lds_dwordx4 v[224:225], off
	v_lshl_add_u64 v[224:225], s[38:39], 0, v[210:211]
	s_mov_b32 m0, s40
	v_lshl_add_u64 v[204:205], v[204:205], 0, s[36:37]
	global_load_lds_dwordx4 v[224:225], off
	v_lshl_add_u64 v[224:225], s[38:39], 0, v[208:209]
	s_add_i32 m0, s40, 0x2000
	s_nop 0
	global_load_lds_dwordx4 v[224:225], off
	v_lshl_add_u64 v[224:225], v[248:249], 0, s[36:37]
	s_mov_b32 m0, s54
	s_nop 0
	global_load_lds_dwordx4 v[224:225], off
	s_mov_b32 m0, s55
	s_nop 0
	global_load_lds_dwordx4 v[204:205], off
	s_waitcnt vmcnt(8)
	s_waitcnt lgkmcnt(0)
	s_barrier
	s_setprio 1
	s_waitcnt lgkmcnt(0)
	v_mfma_f32_16x16x32_bf16 v[64:67], v[136:139], v[168:171], v[64:67]
	v_mfma_f32_16x16x32_bf16 v[60:63], v[144:147], v[168:171], v[60:63]
	v_mfma_f32_16x16x32_bf16 v[56:59], v[136:139], v[176:179], v[56:59]
	v_mfma_f32_16x16x32_bf16 v[52:55], v[144:147], v[176:179], v[52:55]
	v_mfma_f32_16x16x32_bf16 v[40:43], v[136:139], v[184:187], v[40:43]
	v_mfma_f32_16x16x32_bf16 v[36:39], v[144:147], v[184:187], v[36:39]
	v_mfma_f32_16x16x32_bf16 v[24:27], v[136:139], v[192:195], v[24:27]
	v_mfma_f32_16x16x32_bf16 v[20:23], v[144:147], v[192:195], v[20:23]
	s_setprio 0
	s_setprio 1
	v_mfma_f32_16x16x32_bf16 v[64:67], v[140:143], v[172:175], v[64:67]
	v_mfma_f32_16x16x32_bf16 v[60:63], v[148:151], v[172:175], v[60:63]
	v_mfma_f32_16x16x32_bf16 v[56:59], v[140:143], v[180:183], v[56:59]
	v_mfma_f32_16x16x32_bf16 v[52:55], v[148:151], v[180:183], v[52:55]
	v_mfma_f32_16x16x32_bf16 v[40:43], v[140:143], v[188:191], v[40:43]
	v_mfma_f32_16x16x32_bf16 v[36:39], v[148:151], v[188:191], v[36:39]
	v_mfma_f32_16x16x32_bf16 v[24:27], v[140:143], v[196:199], v[24:27]
	v_mfma_f32_16x16x32_bf16 v[20:23], v[148:151], v[196:199], v[20:23]
	s_setprio 0
	s_setprio 1
	v_mfma_f32_16x16x32_bf16 v[48:51], v[152:155], v[168:171], v[48:51]
	v_mfma_f32_16x16x32_bf16 v[44:47], v[160:163], v[168:171], v[44:47]
	v_mfma_f32_16x16x32_bf16 v[32:35], v[152:155], v[176:179], v[32:35]
	v_mfma_f32_16x16x32_bf16 v[28:31], v[160:163], v[176:179], v[28:31]
	v_mfma_f32_16x16x32_bf16 v[16:19], v[152:155], v[184:187], v[16:19]
	v_mfma_f32_16x16x32_bf16 v[12:15], v[160:163], v[184:187], v[12:15]
	v_mfma_f32_16x16x32_bf16 v[8:11], v[152:155], v[192:195], v[8:11]
	v_mfma_f32_16x16x32_bf16 v[4:7], v[160:163], v[192:195], v[4:7]
	s_setprio 0
	s_setprio 1
	v_mfma_f32_16x16x32_bf16 v[48:51], v[156:159], v[172:175], v[48:51]
	v_mfma_f32_16x16x32_bf16 v[44:47], v[164:167], v[172:175], v[44:47]
	v_mfma_f32_16x16x32_bf16 v[32:35], v[156:159], v[180:183], v[32:35]
	v_mfma_f32_16x16x32_bf16 v[28:31], v[164:167], v[180:183], v[28:31]
	v_mfma_f32_16x16x32_bf16 v[16:19], v[156:159], v[188:191], v[16:19]
	v_mfma_f32_16x16x32_bf16 v[12:15], v[164:167], v[188:191], v[12:15]
	v_mfma_f32_16x16x32_bf16 v[8:11], v[156:159], v[196:199], v[8:11]
	v_mfma_f32_16x16x32_bf16 v[4:7], v[164:167], v[196:199], v[4:7]
	s_setprio 0
	s_barrier
	s_add_i32 s61, s61, 2
	s_add_u32 s59, s59, 0x10000
	s_addc_u32 s60, s60, 0
	s_add_u32 s14, s14, 0x100
	s_addc_u32 s15, s15, 0
	s_cmp_gt_u32 s61, 29
	s_cbranch_scc1 .LBB0_838

.LBB0_1175:
	s_waitcnt vmcnt(8)
	s_waitcnt lgkmcnt(0)
	s_barrier
	s_setprio 1
	s_waitcnt lgkmcnt(0)
	v_mfma_f32_16x16x32_bf16 v[132:135], v[152:155], v[180:183], v[132:135]
	v_mfma_f32_16x16x32_bf16 v[128:131], v[160:163], v[180:183], v[128:131]
	v_mfma_f32_16x16x32_bf16 v[124:127], v[152:155], v[176:179], v[124:127]
	v_mfma_f32_16x16x32_bf16 v[120:123], v[160:163], v[176:179], v[120:123]
	v_mfma_f32_16x16x32_bf16 v[116:119], v[152:155], v[172:175], v[116:119]
	v_mfma_f32_16x16x32_bf16 v[112:115], v[160:163], v[172:175], v[112:115]
	v_mfma_f32_16x16x32_bf16 v[108:111], v[152:155], v[168:171], v[108:111]
	v_mfma_f32_16x16x32_bf16 v[104:107], v[160:163], v[168:171], v[104:107]
	s_setprio 0
	s_setprio 1
	v_mfma_f32_16x16x32_bf16 v[132:135], v[156:159], v[196:199], v[132:135]
	v_mfma_f32_16x16x32_bf16 v[128:131], v[164:167], v[196:199], v[128:131]
	v_mfma_f32_16x16x32_bf16 v[124:127], v[156:159], v[192:195], v[124:127]
	v_mfma_f32_16x16x32_bf16 v[120:123], v[164:167], v[192:195], v[120:123]
	v_mfma_f32_16x16x32_bf16 v[116:119], v[156:159], v[188:191], v[116:119]
	v_mfma_f32_16x16x32_bf16 v[112:115], v[164:167], v[188:191], v[112:115]
	v_mfma_f32_16x16x32_bf16 v[108:111], v[156:159], v[184:187], v[108:111]
	v_mfma_f32_16x16x32_bf16 v[104:107], v[164:167], v[184:187], v[104:107]
	s_setprio 0
	s_setprio 1
	v_mfma_f32_16x16x32_bf16 v[100:103], v[136:139], v[180:183], v[100:103]
	v_mfma_f32_16x16x32_bf16 v[96:99], v[144:147], v[180:183], v[96:99]
	v_mfma_f32_16x16x32_bf16 v[92:95], v[136:139], v[176:179], v[92:95]
	v_mfma_f32_16x16x32_bf16 v[88:91], v[144:147], v[176:179], v[88:91]
	v_mfma_f32_16x16x32_bf16 v[80:83], v[136:139], v[172:175], v[80:83]
	v_mfma_f32_16x16x32_bf16 v[76:79], v[144:147], v[172:175], v[76:79]
	v_mfma_f32_16x16x32_bf16 v[72:75], v[136:139], v[168:171], v[72:75]
	v_mfma_f32_16x16x32_bf16 v[68:71], v[144:147], v[168:171], v[68:71]
	s_setprio 0
	s_setprio 1
	v_mfma_f32_16x16x32_bf16 v[100:103], v[140:143], v[196:199], v[100:103]
	v_mfma_f32_16x16x32_bf16 v[96:99], v[148:151], v[196:199], v[96:99]
	v_mfma_f32_16x16x32_bf16 v[92:95], v[140:143], v[192:195], v[92:95]
	v_mfma_f32_16x16x32_bf16 v[88:91], v[148:151], v[192:195], v[88:91]
	v_mfma_f32_16x16x32_bf16 v[80:83], v[140:143], v[188:191], v[80:83]
	v_mfma_f32_16x16x32_bf16 v[76:79], v[148:151], v[188:191], v[76:79]
	v_mfma_f32_16x16x32_bf16 v[72:75], v[140:143], v[184:187], v[72:75]
	v_mfma_f32_16x16x32_bf16 v[68:71], v[148:151], v[184:187], v[68:71]
	s_setprio 0
	s_barrier
	v_cndmask_b32_e64 v200, 0, 1, s[2:3]
	v_cmp_ne_u32_e64 s[4:5], 1, v200
	s_andn2_b64 vcc, exec, s[2:3]
	s_cbranch_vccnz .LBB0_1177
	ds_read_b128 v[180:183], v225 offset:16384
	ds_read_b128 v[196:199], v225 offset:17408
	ds_read_b128 v[176:179], v225 offset:18432
	ds_read_b128 v[192:195], v225 offset:19456
	ds_read_b128 v[172:175], v225 offset:20480
	ds_read_b128 v[188:191], v225 offset:21504
	ds_read_b128 v[168:171], v225 offset:22528
	ds_read_b128 v[184:187], v225 offset:23552
.LBB0_1177:
	s_add_u32 s56, s52, 0x80
	s_addc_u32 s57, s53, 0
	s_and_b64 s[54:55], s[54:55], exec
	s_cselect_b32 s55, s11, s81
	s_cselect_b32 s54, s41, s80
	s_mov_b32 m0, s61
	s_cselect_b32 s57, s23, s57
	s_cselect_b32 s56, s22, s56
	v_lshl_add_u64 v[204:205], s[54:55], 0, v[208:209]
	s_add_u32 s84, s54, 0x4000
	global_load_lds_dwordx4 v[204:205], off
	v_lshl_add_u64 v[204:205], s[54:55], 0, v[210:211]
	s_mov_b32 m0, s62
	s_addc_u32 s85, s55, 0
	global_load_lds_dwordx4 v[204:205], off
	v_lshl_add_u64 v[204:205], s[84:85], 0, v[208:209]
	s_mov_b32 m0, s63
	s_and_b64 vcc, exec, s[4:5]
	global_load_lds_dwordx4 v[204:205], off
	v_lshl_add_u64 v[204:205], s[84:85], 0, v[210:211]
	s_mov_b32 m0, s64
	s_nop 0
	global_load_lds_dwordx4 v[204:205], off
	s_mov_b32 m0, s9
	s_nop 0
	global_load_lds_dwordx4 v2, s[56:57]
	s_mov_b32 m0, s65
	s_nop 0
	global_load_lds_dwordx4 v212, s[56:57]
	s_waitcnt vmcnt(8)
	s_waitcnt lgkmcnt(0)
	s_barrier
	s_cbranch_vccnz .LBB0_1179
	s_setprio 1
	s_waitcnt lgkmcnt(0)
	v_mfma_f32_16x16x32_bf16 v[64:67], v[152:155], v[180:183], v[64:67]
	v_mfma_f32_16x16x32_bf16 v[60:63], v[160:163], v[180:183], v[60:63]
	v_mfma_f32_16x16x32_bf16 v[56:59], v[152:155], v[176:179], v[56:59]
	v_mfma_f32_16x16x32_bf16 v[52:55], v[160:163], v[176:179], v[52:55]
	v_mfma_f32_16x16x32_bf16 v[48:51], v[152:155], v[172:175], v[48:51]
	v_mfma_f32_16x16x32_bf16 v[44:47], v[160:163], v[172:175], v[44:47]
	v_mfma_f32_16x16x32_bf16 v[40:43], v[152:155], v[168:171], v[40:43]
	v_mfma_f32_16x16x32_bf16 v[36:39], v[160:163], v[168:171], v[36:39]
	s_setprio 0
	s_setprio 1
	v_mfma_f32_16x16x32_bf16 v[64:67], v[156:159], v[196:199], v[64:67]
	v_mfma_f32_16x16x32_bf16 v[60:63], v[164:167], v[196:199], v[60:63]
	v_mfma_f32_16x16x32_bf16 v[56:59], v[156:159], v[192:195], v[56:59]
	v_mfma_f32_16x16x32_bf16 v[52:55], v[164:167], v[192:195], v[52:55]
	v_mfma_f32_16x16x32_bf16 v[48:51], v[156:159], v[188:191], v[48:51]
	v_mfma_f32_16x16x32_bf16 v[44:47], v[164:167], v[188:191], v[44:47]
	v_mfma_f32_16x16x32_bf16 v[40:43], v[156:159], v[184:187], v[40:43]
	v_mfma_f32_16x16x32_bf16 v[36:39], v[164:167], v[184:187], v[36:39]
	s_setprio 0
	s_setprio 1
	v_mfma_f32_16x16x32_bf16 v[32:35], v[136:139], v[180:183], v[32:35]
	v_mfma_f32_16x16x32_bf16 v[28:31], v[144:147], v[180:183], v[28:31]
	v_mfma_f32_16x16x32_bf16 v[24:27], v[136:139], v[176:179], v[24:27]
	v_mfma_f32_16x16x32_bf16 v[20:23], v[144:147], v[176:179], v[20:23]
	v_mfma_f32_16x16x32_bf16 v[16:19], v[136:139], v[172:175], v[16:19]
	v_mfma_f32_16x16x32_bf16 v[12:15], v[144:147], v[172:175], v[12:15]
	v_mfma_f32_16x16x32_bf16 v[8:11], v[136:139], v[168:171], v[8:11]
	v_mfma_f32_16x16x32_bf16 v[4:7], v[144:147], v[168:171], v[4:7]
	s_setprio 0
	s_setprio 1
	v_mfma_f32_16x16x32_bf16 v[32:35], v[140:143], v[196:199], v[32:35]
	v_mfma_f32_16x16x32_bf16 v[28:31], v[148:151], v[196:199], v[28:31]
	v_mfma_f32_16x16x32_bf16 v[24:27], v[140:143], v[192:195], v[24:27]
	v_mfma_f32_16x16x32_bf16 v[20:23], v[148:151], v[192:195], v[20:23]
	v_mfma_f32_16x16x32_bf16 v[16:19], v[140:143], v[188:191], v[16:19]
	v_mfma_f32_16x16x32_bf16 v[12:15], v[148:151], v[188:191], v[12:15]
	v_mfma_f32_16x16x32_bf16 v[8:11], v[140:143], v[184:187], v[8:11]
	v_mfma_f32_16x16x32_bf16 v[4:7], v[148:151], v[184:187], v[4:7]
	s_setprio 0
.LBB0_1179:
	s_barrier
	v_add_u32_e32 v136, 0x18000, v224
	v_add_u32_e32 v148, 0x1c000, v224
	ds_read_b128 v[152:155], v136
	ds_read_b128 v[156:159], v136 offset:1024
	ds_read_b128 v[160:163], v136 offset:2048
	ds_read_b128 v[164:167], v136 offset:3072
	ds_read_b128 v[136:139], v148
	ds_read_b128 v[140:143], v148 offset:1024
	ds_read_b128 v[144:147], v148 offset:2048
	ds_read_b128 v[148:151], v148 offset:3072
	s_mov_b32 m0, s66
	s_waitcnt lgkmcnt(0)
	ds_read_b128 v[180:183], v225 offset:32768
	ds_read_b128 v[196:199], v225 offset:33792
	ds_read_b128 v[176:179], v225 offset:34816
	ds_read_b128 v[192:195], v225 offset:35840
	ds_read_b128 v[172:175], v225 offset:36864
	ds_read_b128 v[188:191], v225 offset:37888
	ds_read_b128 v[168:171], v225 offset:38912
	ds_read_b128 v[184:187], v225 offset:39936
	global_load_lds_dwordx4 v218, s[56:57]
	s_mov_b32 m0, s67
	s_nop 0
	global_load_lds_dwordx4 v220, s[56:57]
	s_waitcnt vmcnt(8)
	s_waitcnt lgkmcnt(0)
	s_barrier
	s_setprio 1
	s_waitcnt lgkmcnt(0)
	v_mfma_f32_16x16x32_bf16 v[132:135], v[152:155], v[180:183], v[132:135]
	v_mfma_f32_16x16x32_bf16 v[128:131], v[160:163], v[180:183], v[128:131]
	v_mfma_f32_16x16x32_bf16 v[124:127], v[152:155], v[176:179], v[124:127]
	v_mfma_f32_16x16x32_bf16 v[120:123], v[160:163], v[176:179], v[120:123]
	v_mfma_f32_16x16x32_bf16 v[116:119], v[152:155], v[172:175], v[116:119]
	v_mfma_f32_16x16x32_bf16 v[112:115], v[160:163], v[172:175], v[112:115]
	v_mfma_f32_16x16x32_bf16 v[108:111], v[152:155], v[168:171], v[108:111]
	v_mfma_f32_16x16x32_bf16 v[104:107], v[160:163], v[168:171], v[104:107]
	s_setprio 0
	s_setprio 1
	v_mfma_f32_16x16x32_bf16 v[132:135], v[156:159], v[196:199], v[132:135]
	v_mfma_f32_16x16x32_bf16 v[128:131], v[164:167], v[196:199], v[128:131]
	v_mfma_f32_16x16x32_bf16 v[124:127], v[156:159], v[192:195], v[124:127]
	v_mfma_f32_16x16x32_bf16 v[120:123], v[164:167], v[192:195], v[120:123]
	v_mfma_f32_16x16x32_bf16 v[116:119], v[156:159], v[188:191], v[116:119]
	v_mfma_f32_16x16x32_bf16 v[112:115], v[164:167], v[188:191], v[112:115]
	v_mfma_f32_16x16x32_bf16 v[108:111], v[156:159], v[184:187], v[108:111]
	v_mfma_f32_16x16x32_bf16 v[104:107], v[164:167], v[184:187], v[104:107]
	s_setprio 0
	s_setprio 1
	v_mfma_f32_16x16x32_bf16 v[100:103], v[136:139], v[180:183], v[100:103]
	v_mfma_f32_16x16x32_bf16 v[96:99], v[144:147], v[180:183], v[96:99]
	v_mfma_f32_16x16x32_bf16 v[92:95], v[136:139], v[176:179], v[92:95]
	v_mfma_f32_16x16x32_bf16 v[88:91], v[144:147], v[176:179], v[88:91]
	v_mfma_f32_16x16x32_bf16 v[80:83], v[136:139], v[172:175], v[80:83]
	v_mfma_f32_16x16x32_bf16 v[76:79], v[144:147], v[172:175], v[76:79]
	v_mfma_f32_16x16x32_bf16 v[72:75], v[136:139], v[168:171], v[72:75]
	v_mfma_f32_16x16x32_bf16 v[68:71], v[144:147], v[168:171], v[68:71]
	s_setprio 0
	s_setprio 1
	v_mfma_f32_16x16x32_bf16 v[100:103], v[140:143], v[196:199], v[100:103]
	v_mfma_f32_16x16x32_bf16 v[96:99], v[148:151], v[196:199], v[96:99]
	v_mfma_f32_16x16x32_bf16 v[92:95], v[140:143], v[192:195], v[92:95]
	v_mfma_f32_16x16x32_bf16 v[88:91], v[148:151], v[192:195], v[88:91]
	v_mfma_f32_16x16x32_bf16 v[80:83], v[140:143], v[188:191], v[80:83]
	v_mfma_f32_16x16x32_bf16 v[76:79], v[148:151], v[188:191], v[76:79]
	v_mfma_f32_16x16x32_bf16 v[72:75], v[140:143], v[184:187], v[72:75]
	v_mfma_f32_16x16x32_bf16 v[68:71], v[148:151], v[184:187], v[68:71]
	s_setprio 0
	s_barrier
	s_and_b64 vcc, exec, s[4:5]
	s_cbranch_vccnz .LBB0_1181
	ds_read_b128 v[180:183], v225 offset:49152
	ds_read_b128 v[196:199], v225 offset:50176
	ds_read_b128 v[176:179], v225 offset:51200
	ds_read_b128 v[192:195], v225 offset:52224
	ds_read_b128 v[172:175], v225 offset:53248
	ds_read_b128 v[188:191], v225 offset:54272
	ds_read_b128 v[168:171], v225 offset:55296
	ds_read_b128 v[184:187], v225 offset:56320
.LBB0_1181:
	v_mov_b32_e32 v213, v3
	v_lshl_add_u64 v[204:205], s[56:57], 0, v[2:3]
	v_lshl_add_u64 v[240:241], s[56:57], 0, v[212:213]
	s_add_u32 s56, s54, 0x8000
	s_addc_u32 s57, s55, 0
	s_mov_b32 m0, s69
	v_lshl_add_u64 v[242:243], s[56:57], 0, v[208:209]
	s_add_u32 s54, s54, 0xc000
	global_load_lds_dwordx4 v[242:243], off
	v_lshl_add_u64 v[242:243], s[56:57], 0, v[210:211]
	s_mov_b32 m0, s70
	s_addc_u32 s55, s55, 0
	global_load_lds_dwordx4 v[242:243], off
	v_lshl_add_u64 v[242:243], s[54:55], 0, v[208:209]
	s_mov_b32 m0, s73
	v_lshl_add_u64 v[204:205], v[204:205], 0, s[36:37]
	global_load_lds_dwordx4 v[242:243], off
	v_lshl_add_u64 v[242:243], s[54:55], 0, v[210:211]
	s_mov_b32 m0, s74
	s_and_b64 vcc, exec, s[4:5]
	global_load_lds_dwordx4 v[242:243], off
	s_mov_b32 m0, s71
	s_nop 0
	global_load_lds_dwordx4 v[204:205], off
	v_lshl_add_u64 v[204:205], v[240:241], 0, s[36:37]
	s_mov_b32 m0, s72
	s_nop 0
	global_load_lds_dwordx4 v[204:205], off
	s_waitcnt vmcnt(8)
	s_waitcnt lgkmcnt(0)
	s_barrier
	s_cbranch_vccnz .LBB0_1164
	s_setprio 1
	s_waitcnt lgkmcnt(0)
	v_mfma_f32_16x16x32_bf16 v[64:67], v[152:155], v[180:183], v[64:67]
	v_mfma_f32_16x16x32_bf16 v[60:63], v[160:163], v[180:183], v[60:63]
	v_mfma_f32_16x16x32_bf16 v[56:59], v[152:155], v[176:179], v[56:59]
	v_mfma_f32_16x16x32_bf16 v[52:55], v[160:163], v[176:179], v[52:55]
	v_mfma_f32_16x16x32_bf16 v[48:51], v[152:155], v[172:175], v[48:51]
	v_mfma_f32_16x16x32_bf16 v[44:47], v[160:163], v[172:175], v[44:47]
	v_mfma_f32_16x16x32_bf16 v[40:43], v[152:155], v[168:171], v[40:43]
	v_mfma_f32_16x16x32_bf16 v[36:39], v[160:163], v[168:171], v[36:39]
	s_setprio 0
	s_setprio 1
	v_mfma_f32_16x16x32_bf16 v[64:67], v[156:159], v[196:199], v[64:67]
	v_mfma_f32_16x16x32_bf16 v[60:63], v[164:167], v[196:199], v[60:63]
	v_mfma_f32_16x16x32_bf16 v[56:59], v[156:159], v[192:195], v[56:59]
	v_mfma_f32_16x16x32_bf16 v[52:55], v[164:167], v[192:195], v[52:55]
	v_mfma_f32_16x16x32_bf16 v[48:51], v[156:159], v[188:191], v[48:51]
	v_mfma_f32_16x16x32_bf16 v[44:47], v[164:167], v[188:191], v[44:47]
	v_mfma_f32_16x16x32_bf16 v[40:43], v[156:159], v[184:187], v[40:43]
	v_mfma_f32_16x16x32_bf16 v[36:39], v[164:167], v[184:187], v[36:39]
	s_setprio 0
	s_setprio 1
	v_mfma_f32_16x16x32_bf16 v[32:35], v[136:139], v[180:183], v[32:35]
	v_mfma_f32_16x16x32_bf16 v[28:31], v[144:147], v[180:183], v[28:31]
	v_mfma_f32_16x16x32_bf16 v[24:27], v[136:139], v[176:179], v[24:27]
	v_mfma_f32_16x16x32_bf16 v[20:23], v[144:147], v[176:179], v[20:23]
	v_mfma_f32_16x16x32_bf16 v[16:19], v[136:139], v[172:175], v[16:19]
	v_mfma_f32_16x16x32_bf16 v[12:15], v[144:147], v[172:175], v[12:15]
	v_mfma_f32_16x16x32_bf16 v[8:11], v[136:139], v[168:171], v[8:11]
	v_mfma_f32_16x16x32_bf16 v[4:7], v[144:147], v[168:171], v[4:7]
	s_setprio 0
	s_setprio 1
	v_mfma_f32_16x16x32_bf16 v[32:35], v[140:143], v[196:199], v[32:35]
	v_mfma_f32_16x16x32_bf16 v[28:31], v[148:151], v[196:199], v[28:31]
	v_mfma_f32_16x16x32_bf16 v[24:27], v[140:143], v[192:195], v[24:27]
	v_mfma_f32_16x16x32_bf16 v[20:23], v[148:151], v[192:195], v[20:23]
	v_mfma_f32_16x16x32_bf16 v[16:19], v[140:143], v[188:191], v[16:19]
	v_mfma_f32_16x16x32_bf16 v[12:15], v[148:151], v[188:191], v[12:15]
	v_mfma_f32_16x16x32_bf16 v[8:11], v[140:143], v[184:187], v[8:11]
	v_mfma_f32_16x16x32_bf16 v[4:7], v[148:151], v[184:187], v[4:7]
	s_setprio 0
	s_branch .LBB0_1164

.LBB0_1311:
	s_waitcnt vmcnt(8)
	s_waitcnt lgkmcnt(0)
	s_barrier
	s_setprio 1
	s_waitcnt lgkmcnt(0)
	v_mfma_f32_16x16x32_bf16 v[132:135], v[152:155], v[180:183], v[132:135]
	v_mfma_f32_16x16x32_bf16 v[128:131], v[160:163], v[180:183], v[128:131]
	v_mfma_f32_16x16x32_bf16 v[124:127], v[152:155], v[176:179], v[124:127]
	v_mfma_f32_16x16x32_bf16 v[120:123], v[160:163], v[176:179], v[120:123]
	v_mfma_f32_16x16x32_bf16 v[116:119], v[152:155], v[172:175], v[116:119]
	v_mfma_f32_16x16x32_bf16 v[112:115], v[160:163], v[172:175], v[112:115]
	v_mfma_f32_16x16x32_bf16 v[108:111], v[152:155], v[168:171], v[108:111]
	v_mfma_f32_16x16x32_bf16 v[104:107], v[160:163], v[168:171], v[104:107]
	s_setprio 0
	s_setprio 1
	v_mfma_f32_16x16x32_bf16 v[132:135], v[156:159], v[196:199], v[132:135]
	v_mfma_f32_16x16x32_bf16 v[128:131], v[164:167], v[196:199], v[128:131]
	v_mfma_f32_16x16x32_bf16 v[124:127], v[156:159], v[192:195], v[124:127]
	v_mfma_f32_16x16x32_bf16 v[120:123], v[164:167], v[192:195], v[120:123]
	v_mfma_f32_16x16x32_bf16 v[116:119], v[156:159], v[188:191], v[116:119]
	v_mfma_f32_16x16x32_bf16 v[112:115], v[164:167], v[188:191], v[112:115]
	v_mfma_f32_16x16x32_bf16 v[108:111], v[156:159], v[184:187], v[108:111]
	v_mfma_f32_16x16x32_bf16 v[104:107], v[164:167], v[184:187], v[104:107]
	s_setprio 0
	s_setprio 1
	v_mfma_f32_16x16x32_bf16 v[100:103], v[136:139], v[180:183], v[100:103]
	v_mfma_f32_16x16x32_bf16 v[96:99], v[144:147], v[180:183], v[96:99]
	v_mfma_f32_16x16x32_bf16 v[92:95], v[136:139], v[176:179], v[92:95]
	v_mfma_f32_16x16x32_bf16 v[88:91], v[144:147], v[176:179], v[88:91]
	v_mfma_f32_16x16x32_bf16 v[80:83], v[136:139], v[172:175], v[80:83]
	v_mfma_f32_16x16x32_bf16 v[76:79], v[144:147], v[172:175], v[76:79]
	v_mfma_f32_16x16x32_bf16 v[72:75], v[136:139], v[168:171], v[72:75]
	v_mfma_f32_16x16x32_bf16 v[68:71], v[144:147], v[168:171], v[68:71]
	s_setprio 0
	s_setprio 1
	v_mfma_f32_16x16x32_bf16 v[100:103], v[140:143], v[196:199], v[100:103]
	v_mfma_f32_16x16x32_bf16 v[96:99], v[148:151], v[196:199], v[96:99]
	v_mfma_f32_16x16x32_bf16 v[92:95], v[140:143], v[192:195], v[92:95]
	v_mfma_f32_16x16x32_bf16 v[88:91], v[148:151], v[192:195], v[88:91]
	v_mfma_f32_16x16x32_bf16 v[80:83], v[140:143], v[188:191], v[80:83]
	v_mfma_f32_16x16x32_bf16 v[76:79], v[148:151], v[188:191], v[76:79]
	v_mfma_f32_16x16x32_bf16 v[72:75], v[140:143], v[184:187], v[72:75]
	v_mfma_f32_16x16x32_bf16 v[68:71], v[148:151], v[184:187], v[68:71]
	s_setprio 0
	s_barrier
	v_cndmask_b32_e64 v200, 0, 1, s[2:3]
	v_cmp_ne_u32_e64 s[4:5], 1, v200
	s_andn2_b64 vcc, exec, s[2:3]
	s_cbranch_vccnz .LBB0_1313
	ds_read_b128 v[180:183], v242 offset:16384
	ds_read_b128 v[196:199], v242 offset:17408
	ds_read_b128 v[176:179], v242 offset:18432
	ds_read_b128 v[192:195], v242 offset:19456
	ds_read_b128 v[172:175], v242 offset:20480
	ds_read_b128 v[188:191], v242 offset:21504
	ds_read_b128 v[168:171], v242 offset:22528
	ds_read_b128 v[184:187], v242 offset:23552
.LBB0_1313:
	s_add_u32 s56, s52, 0x80
	s_addc_u32 s57, s53, 0
	s_and_b64 s[54:55], s[54:55], exec
	s_cselect_b32 s55, s41, s83
	s_cselect_b32 s54, s43, s82
	s_mov_b32 m0, s65
	s_cselect_b32 s57, s25, s57
	s_cselect_b32 s56, s24, s56
	v_lshl_add_u64 v[204:205], s[54:55], 0, v[208:209]
	s_add_u32 s86, s54, 0x4000
	global_load_lds_dwordx4 v[204:205], off
	v_lshl_add_u64 v[204:205], s[54:55], 0, v[210:211]
	s_mov_b32 m0, s66
	s_addc_u32 s87, s55, 0
	global_load_lds_dwordx4 v[204:205], off
	v_lshl_add_u64 v[204:205], s[86:87], 0, v[208:209]
	s_mov_b32 m0, s67
	s_and_b64 vcc, exec, s[4:5]
	global_load_lds_dwordx4 v[204:205], off
	v_lshl_add_u64 v[204:205], s[86:87], 0, v[210:211]
	s_mov_b32 m0, s68
	s_nop 0
	global_load_lds_dwordx4 v[204:205], off
	s_mov_b32 m0, s11
	s_nop 0
	global_load_lds_dwordx4 v2, s[56:57]
	s_mov_b32 m0, s69
	s_nop 0
	global_load_lds_dwordx4 v212, s[56:57]
	s_waitcnt vmcnt(8)
	s_waitcnt lgkmcnt(0)
	s_barrier
	s_cbranch_vccnz .LBB0_1315
	s_setprio 1
	s_waitcnt lgkmcnt(0)
	v_mfma_f32_16x16x32_bf16 v[64:67], v[152:155], v[180:183], v[64:67]
	v_mfma_f32_16x16x32_bf16 v[60:63], v[160:163], v[180:183], v[60:63]
	v_mfma_f32_16x16x32_bf16 v[56:59], v[152:155], v[176:179], v[56:59]
	v_mfma_f32_16x16x32_bf16 v[52:55], v[160:163], v[176:179], v[52:55]
	v_mfma_f32_16x16x32_bf16 v[48:51], v[152:155], v[172:175], v[48:51]
	v_mfma_f32_16x16x32_bf16 v[44:47], v[160:163], v[172:175], v[44:47]
	v_mfma_f32_16x16x32_bf16 v[40:43], v[152:155], v[168:171], v[40:43]
	v_mfma_f32_16x16x32_bf16 v[36:39], v[160:163], v[168:171], v[36:39]
	s_setprio 0
	s_setprio 1
	v_mfma_f32_16x16x32_bf16 v[64:67], v[156:159], v[196:199], v[64:67]
	v_mfma_f32_16x16x32_bf16 v[60:63], v[164:167], v[196:199], v[60:63]
	v_mfma_f32_16x16x32_bf16 v[56:59], v[156:159], v[192:195], v[56:59]
	v_mfma_f32_16x16x32_bf16 v[52:55], v[164:167], v[192:195], v[52:55]
	v_mfma_f32_16x16x32_bf16 v[48:51], v[156:159], v[188:191], v[48:51]
	v_mfma_f32_16x16x32_bf16 v[44:47], v[164:167], v[188:191], v[44:47]
	v_mfma_f32_16x16x32_bf16 v[40:43], v[156:159], v[184:187], v[40:43]
	v_mfma_f32_16x16x32_bf16 v[36:39], v[164:167], v[184:187], v[36:39]
	s_setprio 0
	s_setprio 1
	v_mfma_f32_16x16x32_bf16 v[32:35], v[136:139], v[180:183], v[32:35]
	v_mfma_f32_16x16x32_bf16 v[28:31], v[144:147], v[180:183], v[28:31]
	v_mfma_f32_16x16x32_bf16 v[24:27], v[136:139], v[176:179], v[24:27]
	v_mfma_f32_16x16x32_bf16 v[20:23], v[144:147], v[176:179], v[20:23]
	v_mfma_f32_16x16x32_bf16 v[16:19], v[136:139], v[172:175], v[16:19]
	v_mfma_f32_16x16x32_bf16 v[12:15], v[144:147], v[172:175], v[12:15]
	v_mfma_f32_16x16x32_bf16 v[8:11], v[136:139], v[168:171], v[8:11]
	v_mfma_f32_16x16x32_bf16 v[4:7], v[144:147], v[168:171], v[4:7]
	s_setprio 0
	s_setprio 1
	v_mfma_f32_16x16x32_bf16 v[32:35], v[140:143], v[196:199], v[32:35]
	v_mfma_f32_16x16x32_bf16 v[28:31], v[148:151], v[196:199], v[28:31]
	v_mfma_f32_16x16x32_bf16 v[24:27], v[140:143], v[192:195], v[24:27]
	v_mfma_f32_16x16x32_bf16 v[20:23], v[148:151], v[192:195], v[20:23]
	v_mfma_f32_16x16x32_bf16 v[16:19], v[140:143], v[188:191], v[16:19]
	v_mfma_f32_16x16x32_bf16 v[12:15], v[148:151], v[188:191], v[12:15]
	v_mfma_f32_16x16x32_bf16 v[8:11], v[140:143], v[184:187], v[8:11]
	v_mfma_f32_16x16x32_bf16 v[4:7], v[148:151], v[184:187], v[4:7]
	s_setprio 0
.LBB0_1315:
	s_barrier
	v_add_u32_e32 v136, 0x18000, v241
	v_add_u32_e32 v148, 0x1c000, v241
	ds_read_b128 v[152:155], v136
	ds_read_b128 v[156:159], v136 offset:1024
	ds_read_b128 v[160:163], v136 offset:2048
	ds_read_b128 v[164:167], v136 offset:3072
	ds_read_b128 v[136:139], v148
	ds_read_b128 v[140:143], v148 offset:1024
	ds_read_b128 v[144:147], v148 offset:2048
	ds_read_b128 v[148:151], v148 offset:3072
	s_mov_b32 m0, s70
	s_waitcnt lgkmcnt(0)
	ds_read_b128 v[180:183], v242 offset:32768
	ds_read_b128 v[196:199], v242 offset:33792
	ds_read_b128 v[176:179], v242 offset:34816
	ds_read_b128 v[192:195], v242 offset:35840
	ds_read_b128 v[172:175], v242 offset:36864
	ds_read_b128 v[188:191], v242 offset:37888
	ds_read_b128 v[168:171], v242 offset:38912
	ds_read_b128 v[184:187], v242 offset:39936
	global_load_lds_dwordx4 v218, s[56:57]
	s_mov_b32 m0, s71
	s_nop 0
	global_load_lds_dwordx4 v219, s[56:57]
	s_waitcnt vmcnt(8)
	s_waitcnt lgkmcnt(0)
	s_barrier
	s_setprio 1
	s_waitcnt lgkmcnt(0)
	v_mfma_f32_16x16x32_bf16 v[132:135], v[152:155], v[180:183], v[132:135]
	v_mfma_f32_16x16x32_bf16 v[128:131], v[160:163], v[180:183], v[128:131]
	v_mfma_f32_16x16x32_bf16 v[124:127], v[152:155], v[176:179], v[124:127]
	v_mfma_f32_16x16x32_bf16 v[120:123], v[160:163], v[176:179], v[120:123]
	v_mfma_f32_16x16x32_bf16 v[116:119], v[152:155], v[172:175], v[116:119]
	v_mfma_f32_16x16x32_bf16 v[112:115], v[160:163], v[172:175], v[112:115]
	v_mfma_f32_16x16x32_bf16 v[108:111], v[152:155], v[168:171], v[108:111]
	v_mfma_f32_16x16x32_bf16 v[104:107], v[160:163], v[168:171], v[104:107]
	s_setprio 0
	s_setprio 1
	v_mfma_f32_16x16x32_bf16 v[132:135], v[156:159], v[196:199], v[132:135]
	v_mfma_f32_16x16x32_bf16 v[128:131], v[164:167], v[196:199], v[128:131]
	v_mfma_f32_16x16x32_bf16 v[124:127], v[156:159], v[192:195], v[124:127]
	v_mfma_f32_16x16x32_bf16 v[120:123], v[164:167], v[192:195], v[120:123]
	v_mfma_f32_16x16x32_bf16 v[116:119], v[156:159], v[188:191], v[116:119]
	v_mfma_f32_16x16x32_bf16 v[112:115], v[164:167], v[188:191], v[112:115]
	v_mfma_f32_16x16x32_bf16 v[108:111], v[156:159], v[184:187], v[108:111]
	v_mfma_f32_16x16x32_bf16 v[104:107], v[164:167], v[184:187], v[104:107]
	s_setprio 0
	s_setprio 1
	v_mfma_f32_16x16x32_bf16 v[100:103], v[136:139], v[180:183], v[100:103]
	v_mfma_f32_16x16x32_bf16 v[96:99], v[144:147], v[180:183], v[96:99]
	v_mfma_f32_16x16x32_bf16 v[92:95], v[136:139], v[176:179], v[92:95]
	v_mfma_f32_16x16x32_bf16 v[88:91], v[144:147], v[176:179], v[88:91]
	v_mfma_f32_16x16x32_bf16 v[80:83], v[136:139], v[172:175], v[80:83]
	v_mfma_f32_16x16x32_bf16 v[76:79], v[144:147], v[172:175], v[76:79]
	v_mfma_f32_16x16x32_bf16 v[72:75], v[136:139], v[168:171], v[72:75]
	v_mfma_f32_16x16x32_bf16 v[68:71], v[144:147], v[168:171], v[68:71]
	s_setprio 0
	s_setprio 1
	v_mfma_f32_16x16x32_bf16 v[100:103], v[140:143], v[196:199], v[100:103]
	v_mfma_f32_16x16x32_bf16 v[96:99], v[148:151], v[196:199], v[96:99]
	v_mfma_f32_16x16x32_bf16 v[92:95], v[140:143], v[192:195], v[92:95]
	v_mfma_f32_16x16x32_bf16 v[88:91], v[148:151], v[192:195], v[88:91]
	v_mfma_f32_16x16x32_bf16 v[80:83], v[140:143], v[188:191], v[80:83]
	v_mfma_f32_16x16x32_bf16 v[76:79], v[148:151], v[188:191], v[76:79]
	v_mfma_f32_16x16x32_bf16 v[72:75], v[140:143], v[184:187], v[72:75]
	v_mfma_f32_16x16x32_bf16 v[68:71], v[148:151], v[184:187], v[68:71]
	s_setprio 0
	s_barrier
	s_and_b64 vcc, exec, s[4:5]
	s_cbranch_vccnz .LBB0_1317
	ds_read_b128 v[180:183], v242 offset:49152
	ds_read_b128 v[196:199], v242 offset:50176
	ds_read_b128 v[176:179], v242 offset:51200
	ds_read_b128 v[192:195], v242 offset:52224
	ds_read_b128 v[172:175], v242 offset:53248
	ds_read_b128 v[188:191], v242 offset:54272
	ds_read_b128 v[168:171], v242 offset:55296
	ds_read_b128 v[184:187], v242 offset:56320
.LBB0_1317:
	v_mov_b32_e32 v213, v3
	v_lshl_add_u64 v[204:205], s[56:57], 0, v[2:3]
	v_lshl_add_u64 v[206:207], s[56:57], 0, v[212:213]
	s_add_u32 s56, s54, 0x8000
	s_addc_u32 s57, s55, 0
	s_mov_b32 m0, s72
	v_lshl_add_u64 v[200:201], s[56:57], 0, v[208:209]
	s_add_u32 s54, s54, 0xc000
	global_load_lds_dwordx4 v[200:201], off
	v_lshl_add_u64 v[200:201], s[56:57], 0, v[210:211]
	s_mov_b32 m0, s73
	s_addc_u32 s55, s55, 0
	global_load_lds_dwordx4 v[200:201], off
	v_lshl_add_u64 v[200:201], s[54:55], 0, v[208:209]
	s_mov_b32 m0, s76
	s_and_b64 vcc, exec, s[4:5]
	global_load_lds_dwordx4 v[200:201], off
	v_lshl_add_u64 v[200:201], s[54:55], 0, v[210:211]
	s_mov_b32 m0, s77
	s_nop 0
	global_load_lds_dwordx4 v[200:201], off
	v_lshl_add_u64 v[200:201], v[204:205], 0, s[36:37]
	s_mov_b32 m0, s74
	s_nop 0
	global_load_lds_dwordx4 v[200:201], off
	v_lshl_add_u64 v[200:201], v[206:207], 0, s[36:37]
	s_mov_b32 m0, s75
	s_nop 0
	global_load_lds_dwordx4 v[200:201], off
	s_waitcnt vmcnt(8)
	s_waitcnt lgkmcnt(0)
	s_barrier
	s_cbranch_vccnz .LBB0_1308
	s_setprio 1
	s_waitcnt lgkmcnt(0)
	v_mfma_f32_16x16x32_bf16 v[64:67], v[152:155], v[180:183], v[64:67]
	v_mfma_f32_16x16x32_bf16 v[60:63], v[160:163], v[180:183], v[60:63]
	v_mfma_f32_16x16x32_bf16 v[56:59], v[152:155], v[176:179], v[56:59]
	v_mfma_f32_16x16x32_bf16 v[52:55], v[160:163], v[176:179], v[52:55]
	v_mfma_f32_16x16x32_bf16 v[48:51], v[152:155], v[172:175], v[48:51]
	v_mfma_f32_16x16x32_bf16 v[44:47], v[160:163], v[172:175], v[44:47]
	v_mfma_f32_16x16x32_bf16 v[40:43], v[152:155], v[168:171], v[40:43]
	v_mfma_f32_16x16x32_bf16 v[36:39], v[160:163], v[168:171], v[36:39]
	s_setprio 0
	s_setprio 1
	v_mfma_f32_16x16x32_bf16 v[64:67], v[156:159], v[196:199], v[64:67]
	v_mfma_f32_16x16x32_bf16 v[60:63], v[164:167], v[196:199], v[60:63]
	v_mfma_f32_16x16x32_bf16 v[56:59], v[156:159], v[192:195], v[56:59]
	v_mfma_f32_16x16x32_bf16 v[52:55], v[164:167], v[192:195], v[52:55]
	v_mfma_f32_16x16x32_bf16 v[48:51], v[156:159], v[188:191], v[48:51]
	v_mfma_f32_16x16x32_bf16 v[44:47], v[164:167], v[188:191], v[44:47]
	v_mfma_f32_16x16x32_bf16 v[40:43], v[156:159], v[184:187], v[40:43]
	v_mfma_f32_16x16x32_bf16 v[36:39], v[164:167], v[184:187], v[36:39]
	s_setprio 0
	s_setprio 1
	v_mfma_f32_16x16x32_bf16 v[32:35], v[136:139], v[180:183], v[32:35]
	v_mfma_f32_16x16x32_bf16 v[28:31], v[144:147], v[180:183], v[28:31]
	v_mfma_f32_16x16x32_bf16 v[24:27], v[136:139], v[176:179], v[24:27]
	v_mfma_f32_16x16x32_bf16 v[20:23], v[144:147], v[176:179], v[20:23]
	v_mfma_f32_16x16x32_bf16 v[16:19], v[136:139], v[172:175], v[16:19]
	v_mfma_f32_16x16x32_bf16 v[12:15], v[144:147], v[172:175], v[12:15]
	v_mfma_f32_16x16x32_bf16 v[8:11], v[136:139], v[168:171], v[8:11]
	v_mfma_f32_16x16x32_bf16 v[4:7], v[144:147], v[168:171], v[4:7]
	s_setprio 0
	s_setprio 1
	v_mfma_f32_16x16x32_bf16 v[32:35], v[140:143], v[196:199], v[32:35]
	v_mfma_f32_16x16x32_bf16 v[28:31], v[148:151], v[196:199], v[28:31]
	v_mfma_f32_16x16x32_bf16 v[24:27], v[140:143], v[192:195], v[24:27]
	v_mfma_f32_16x16x32_bf16 v[20:23], v[148:151], v[192:195], v[20:23]
	v_mfma_f32_16x16x32_bf16 v[16:19], v[140:143], v[188:191], v[16:19]
	v_mfma_f32_16x16x32_bf16 v[12:15], v[148:151], v[188:191], v[12:15]
	v_mfma_f32_16x16x32_bf16 v[8:11], v[140:143], v[184:187], v[8:11]
	v_mfma_f32_16x16x32_bf16 v[4:7], v[148:151], v[184:187], v[4:7]
	s_setprio 0
	s_branch .LBB0_1308

.LBB0_1429:
	s_add_u32 s52, s48, 0x80
	s_addc_u32 s53, s49, 0
	s_and_b64 s[50:51], s[50:51], exec
	s_cselect_b32 s51, s15, s74
	s_cselect_b32 s50, s39, s73
	s_mov_b32 m0, s55
	s_cselect_b32 s53, s25, s53
	s_cselect_b32 s52, s24, s52
	v_lshl_add_u64 v[200:201], s[50:51], 0, v[208:209]
	s_add_u32 s76, s50, 0x4000
	global_load_lds_dwordx4 v[200:201], off
	v_lshl_add_u64 v[200:201], s[50:51], 0, v[210:211]
	s_mov_b32 m0, s56
	s_addc_u32 s77, s51, 0
	global_load_lds_dwordx4 v[200:201], off
	v_lshl_add_u64 v[200:201], s[76:77], 0, v[208:209]
	s_mov_b32 m0, s57
	s_and_b64 vcc, exec, s[4:5]
	global_load_lds_dwordx4 v[200:201], off
	v_lshl_add_u64 v[200:201], s[76:77], 0, v[210:211]
	s_mov_b32 m0, s59
	s_nop 0
	global_load_lds_dwordx4 v[200:201], off
	s_mov_b32 m0, s7
	s_nop 0
	global_load_lds_dwordx4 v2, s[52:53]
	s_mov_b32 m0, s60
	s_nop 0
	global_load_lds_dwordx4 v212, s[52:53]
	s_waitcnt vmcnt(8)
	s_waitcnt lgkmcnt(0)
	s_barrier
	s_cbranch_vccnz .LBB0_1431
	s_setprio 1
	s_waitcnt lgkmcnt(0)
	v_mfma_f32_16x16x32_bf16 v[64:67], v[152:155], v[180:183], v[64:67]
	v_mfma_f32_16x16x32_bf16 v[60:63], v[160:163], v[180:183], v[60:63]
	v_mfma_f32_16x16x32_bf16 v[56:59], v[152:155], v[176:179], v[56:59]
	v_mfma_f32_16x16x32_bf16 v[52:55], v[160:163], v[176:179], v[52:55]
	v_mfma_f32_16x16x32_bf16 v[48:51], v[152:155], v[172:175], v[48:51]
	v_mfma_f32_16x16x32_bf16 v[44:47], v[160:163], v[172:175], v[44:47]
	v_mfma_f32_16x16x32_bf16 v[40:43], v[152:155], v[168:171], v[40:43]
	v_mfma_f32_16x16x32_bf16 v[36:39], v[160:163], v[168:171], v[36:39]
	s_setprio 0
	s_setprio 1
	v_mfma_f32_16x16x32_bf16 v[64:67], v[156:159], v[196:199], v[64:67]
	v_mfma_f32_16x16x32_bf16 v[60:63], v[164:167], v[196:199], v[60:63]
	v_mfma_f32_16x16x32_bf16 v[56:59], v[156:159], v[192:195], v[56:59]
	v_mfma_f32_16x16x32_bf16 v[52:55], v[164:167], v[192:195], v[52:55]
	v_mfma_f32_16x16x32_bf16 v[48:51], v[156:159], v[188:191], v[48:51]
	v_mfma_f32_16x16x32_bf16 v[44:47], v[164:167], v[188:191], v[44:47]
	v_mfma_f32_16x16x32_bf16 v[40:43], v[156:159], v[184:187], v[40:43]
	v_mfma_f32_16x16x32_bf16 v[36:39], v[164:167], v[184:187], v[36:39]
	s_setprio 0
	s_setprio 1
	v_mfma_f32_16x16x32_bf16 v[32:35], v[136:139], v[180:183], v[32:35]
	v_mfma_f32_16x16x32_bf16 v[28:31], v[144:147], v[180:183], v[28:31]
	v_mfma_f32_16x16x32_bf16 v[24:27], v[136:139], v[176:179], v[24:27]
	v_mfma_f32_16x16x32_bf16 v[20:23], v[144:147], v[176:179], v[20:23]
	v_mfma_f32_16x16x32_bf16 v[16:19], v[136:139], v[172:175], v[16:19]
	v_mfma_f32_16x16x32_bf16 v[12:15], v[144:147], v[172:175], v[12:15]
	v_mfma_f32_16x16x32_bf16 v[8:11], v[136:139], v[168:171], v[8:11]
	v_mfma_f32_16x16x32_bf16 v[4:7], v[144:147], v[168:171], v[4:7]
	s_setprio 0
	s_setprio 1
	v_mfma_f32_16x16x32_bf16 v[32:35], v[140:143], v[196:199], v[32:35]
	v_mfma_f32_16x16x32_bf16 v[28:31], v[148:151], v[196:199], v[28:31]
	v_mfma_f32_16x16x32_bf16 v[24:27], v[140:143], v[192:195], v[24:27]
	v_mfma_f32_16x16x32_bf16 v[20:23], v[148:151], v[192:195], v[20:23]
	v_mfma_f32_16x16x32_bf16 v[16:19], v[140:143], v[188:191], v[16:19]
	v_mfma_f32_16x16x32_bf16 v[12:15], v[148:151], v[188:191], v[12:15]
	v_mfma_f32_16x16x32_bf16 v[8:11], v[140:143], v[184:187], v[8:11]
	v_mfma_f32_16x16x32_bf16 v[4:7], v[148:151], v[184:187], v[4:7]
	s_setprio 0
.LBB0_1431:
	s_barrier
	v_add_u32_e32 v136, 0x18000, v241
	v_add_u32_e32 v148, 0x1c000, v241
	ds_read_b128 v[152:155], v136
	ds_read_b128 v[156:159], v136 offset:1024
	ds_read_b128 v[160:163], v136 offset:2048
	ds_read_b128 v[164:167], v136 offset:3072
	ds_read_b128 v[136:139], v148
	ds_read_b128 v[140:143], v148 offset:1024
	ds_read_b128 v[144:147], v148 offset:2048
	ds_read_b128 v[148:151], v148 offset:3072
	s_mov_b32 m0, s61
	s_waitcnt lgkmcnt(0)
	ds_read_b128 v[180:183], v242 offset:32768
	ds_read_b128 v[196:199], v242 offset:33792
	ds_read_b128 v[176:179], v242 offset:34816
	ds_read_b128 v[192:195], v242 offset:35840
	ds_read_b128 v[172:175], v242 offset:36864
	ds_read_b128 v[188:191], v242 offset:37888
	ds_read_b128 v[168:171], v242 offset:38912
	ds_read_b128 v[184:187], v242 offset:39936
	global_load_lds_dwordx4 v218, s[52:53]
	s_mov_b32 m0, s62
	s_nop 0
	global_load_lds_dwordx4 v219, s[52:53]
	s_waitcnt vmcnt(8)
	s_waitcnt lgkmcnt(0)
	s_barrier
	s_setprio 1
	s_waitcnt lgkmcnt(0)
	v_mfma_f32_16x16x32_bf16 v[132:135], v[152:155], v[180:183], v[132:135]
	v_mfma_f32_16x16x32_bf16 v[128:131], v[160:163], v[180:183], v[128:131]
	v_mfma_f32_16x16x32_bf16 v[124:127], v[152:155], v[176:179], v[124:127]
	v_mfma_f32_16x16x32_bf16 v[120:123], v[160:163], v[176:179], v[120:123]
	v_mfma_f32_16x16x32_bf16 v[116:119], v[152:155], v[172:175], v[116:119]
	v_mfma_f32_16x16x32_bf16 v[112:115], v[160:163], v[172:175], v[112:115]
	v_mfma_f32_16x16x32_bf16 v[108:111], v[152:155], v[168:171], v[108:111]
	v_mfma_f32_16x16x32_bf16 v[104:107], v[160:163], v[168:171], v[104:107]
	s_setprio 0
	s_setprio 1
	v_mfma_f32_16x16x32_bf16 v[132:135], v[156:159], v[196:199], v[132:135]
	v_mfma_f32_16x16x32_bf16 v[128:131], v[164:167], v[196:199], v[128:131]
	v_mfma_f32_16x16x32_bf16 v[124:127], v[156:159], v[192:195], v[124:127]
	v_mfma_f32_16x16x32_bf16 v[120:123], v[164:167], v[192:195], v[120:123]
	v_mfma_f32_16x16x32_bf16 v[116:119], v[156:159], v[188:191], v[116:119]
	v_mfma_f32_16x16x32_bf16 v[112:115], v[164:167], v[188:191], v[112:115]
	v_mfma_f32_16x16x32_bf16 v[108:111], v[156:159], v[184:187], v[108:111]
	v_mfma_f32_16x16x32_bf16 v[104:107], v[164:167], v[184:187], v[104:107]
	s_setprio 0
	s_setprio 1
	v_mfma_f32_16x16x32_bf16 v[100:103], v[136:139], v[180:183], v[100:103]
	v_mfma_f32_16x16x32_bf16 v[96:99], v[144:147], v[180:183], v[96:99]
	v_mfma_f32_16x16x32_bf16 v[92:95], v[136:139], v[176:179], v[92:95]
	v_mfma_f32_16x16x32_bf16 v[88:91], v[144:147], v[176:179], v[88:91]
	v_mfma_f32_16x16x32_bf16 v[80:83], v[136:139], v[172:175], v[80:83]
	v_mfma_f32_16x16x32_bf16 v[76:79], v[144:147], v[172:175], v[76:79]
	v_mfma_f32_16x16x32_bf16 v[72:75], v[136:139], v[168:171], v[72:75]
	v_mfma_f32_16x16x32_bf16 v[68:71], v[144:147], v[168:171], v[68:71]
	s_setprio 0
	s_setprio 1
	v_mfma_f32_16x16x32_bf16 v[100:103], v[140:143], v[196:199], v[100:103]
	v_mfma_f32_16x16x32_bf16 v[96:99], v[148:151], v[196:199], v[96:99]
	v_mfma_f32_16x16x32_bf16 v[92:95], v[140:143], v[192:195], v[92:95]
	v_mfma_f32_16x16x32_bf16 v[88:91], v[148:151], v[192:195], v[88:91]
	v_mfma_f32_16x16x32_bf16 v[80:83], v[140:143], v[188:191], v[80:83]
	v_mfma_f32_16x16x32_bf16 v[76:79], v[148:151], v[188:191], v[76:79]
	v_mfma_f32_16x16x32_bf16 v[72:75], v[140:143], v[184:187], v[72:75]
	v_mfma_f32_16x16x32_bf16 v[68:71], v[148:151], v[184:187], v[68:71]
	s_setprio 0
	s_barrier
	s_and_b64 vcc, exec, s[4:5]
	s_cbranch_vccnz .LBB0_1433
	ds_read_b128 v[180:183], v242 offset:49152
	ds_read_b128 v[196:199], v242 offset:50176
	ds_read_b128 v[176:179], v242 offset:51200
	ds_read_b128 v[192:195], v242 offset:52224
	ds_read_b128 v[172:175], v242 offset:53248
	ds_read_b128 v[188:191], v242 offset:54272
	ds_read_b128 v[168:171], v242 offset:55296
	ds_read_b128 v[184:187], v242 offset:56320
.LBB0_1433:
	v_mov_b32_e32 v213, v3
	v_lshl_add_u64 v[200:201], s[52:53], 0, v[2:3]
	v_lshl_add_u64 v[204:205], s[52:53], 0, v[212:213]
	s_add_u32 s52, s50, 0x8000
	s_addc_u32 s53, s51, 0
	s_mov_b32 m0, s63
	v_lshl_add_u64 v[206:207], s[52:53], 0, v[208:209]
	s_add_u32 s50, s50, 0xc000
	global_load_lds_dwordx4 v[206:207], off
	v_lshl_add_u64 v[206:207], s[52:53], 0, v[210:211]
	s_mov_b32 m0, s64
	s_addc_u32 s51, s51, 0
	global_load_lds_dwordx4 v[206:207], off
	v_lshl_add_u64 v[206:207], s[50:51], 0, v[208:209]
	s_mov_b32 m0, s67
	v_lshl_add_u64 v[200:201], v[200:201], 0, s[36:37]
	global_load_lds_dwordx4 v[206:207], off
	v_lshl_add_u64 v[206:207], s[50:51], 0, v[210:211]
	s_mov_b32 m0, s68
	s_and_b64 vcc, exec, s[4:5]
	global_load_lds_dwordx4 v[206:207], off
	s_mov_b32 m0, s65
	s_nop 0
	global_load_lds_dwordx4 v[200:201], off
	v_lshl_add_u64 v[200:201], v[204:205], 0, s[36:37]
	s_mov_b32 m0, s66
	s_nop 0
	global_load_lds_dwordx4 v[200:201], off
	s_waitcnt vmcnt(8)
	s_waitcnt lgkmcnt(0)
	s_barrier
	s_cbranch_vccnz .LBB0_1424
	s_setprio 1
	s_waitcnt lgkmcnt(0)
	v_mfma_f32_16x16x32_bf16 v[64:67], v[152:155], v[180:183], v[64:67]
	v_mfma_f32_16x16x32_bf16 v[60:63], v[160:163], v[180:183], v[60:63]
	v_mfma_f32_16x16x32_bf16 v[56:59], v[152:155], v[176:179], v[56:59]
	v_mfma_f32_16x16x32_bf16 v[52:55], v[160:163], v[176:179], v[52:55]
	v_mfma_f32_16x16x32_bf16 v[48:51], v[152:155], v[172:175], v[48:51]
	v_mfma_f32_16x16x32_bf16 v[44:47], v[160:163], v[172:175], v[44:47]
	v_mfma_f32_16x16x32_bf16 v[40:43], v[152:155], v[168:171], v[40:43]
	v_mfma_f32_16x16x32_bf16 v[36:39], v[160:163], v[168:171], v[36:39]
	s_setprio 0
	s_setprio 1
	v_mfma_f32_16x16x32_bf16 v[64:67], v[156:159], v[196:199], v[64:67]
	v_mfma_f32_16x16x32_bf16 v[60:63], v[164:167], v[196:199], v[60:63]
	v_mfma_f32_16x16x32_bf16 v[56:59], v[156:159], v[192:195], v[56:59]
	v_mfma_f32_16x16x32_bf16 v[52:55], v[164:167], v[192:195], v[52:55]
	v_mfma_f32_16x16x32_bf16 v[48:51], v[156:159], v[188:191], v[48:51]
	v_mfma_f32_16x16x32_bf16 v[44:47], v[164:167], v[188:191], v[44:47]
	v_mfma_f32_16x16x32_bf16 v[40:43], v[156:159], v[184:187], v[40:43]
	v_mfma_f32_16x16x32_bf16 v[36:39], v[164:167], v[184:187], v[36:39]
	s_setprio 0
	s_setprio 1
	v_mfma_f32_16x16x32_bf16 v[32:35], v[136:139], v[180:183], v[32:35]
	v_mfma_f32_16x16x32_bf16 v[28:31], v[144:147], v[180:183], v[28:31]
	v_mfma_f32_16x16x32_bf16 v[24:27], v[136:139], v[176:179], v[24:27]
	v_mfma_f32_16x16x32_bf16 v[20:23], v[144:147], v[176:179], v[20:23]
	v_mfma_f32_16x16x32_bf16 v[16:19], v[136:139], v[172:175], v[16:19]
	v_mfma_f32_16x16x32_bf16 v[12:15], v[144:147], v[172:175], v[12:15]
	v_mfma_f32_16x16x32_bf16 v[8:11], v[136:139], v[168:171], v[8:11]
	v_mfma_f32_16x16x32_bf16 v[4:7], v[144:147], v[168:171], v[4:7]
	s_setprio 0
	s_setprio 1
	v_mfma_f32_16x16x32_bf16 v[32:35], v[140:143], v[196:199], v[32:35]
	v_mfma_f32_16x16x32_bf16 v[28:31], v[148:151], v[196:199], v[28:31]
	v_mfma_f32_16x16x32_bf16 v[24:27], v[140:143], v[192:195], v[24:27]
	v_mfma_f32_16x16x32_bf16 v[20:23], v[148:151], v[192:195], v[20:23]
	v_mfma_f32_16x16x32_bf16 v[16:19], v[140:143], v[188:191], v[16:19]
	v_mfma_f32_16x16x32_bf16 v[12:15], v[148:151], v[188:191], v[12:15]
	v_mfma_f32_16x16x32_bf16 v[8:11], v[140:143], v[184:187], v[8:11]
	v_mfma_f32_16x16x32_bf16 v[4:7], v[148:151], v[184:187], v[4:7]
	s_setprio 0
	s_branch .LBB0_1424
